# retire stage loads at epilogue end with counted vmcnt; first-trip waits no longer drain epilogue stores (INPROJ, KV, WO, DOWN)
# speedup vs baseline: 1.0129x; 1.0022x over previous
.LBB0_87:
	s_andn2_b64 vcc, exec, s[22:23]
	s_cbranch_vccnz .LBB0_90
	s_add_u32 s46, s46, 0x80
	s_addc_u32 s47, s47, 0
	s_add_u32 s27, s48, 0x100
	s_addc_u32 s29, s49, 0
	s_mov_b32 s4, 0
	s_add_i32 s48, s4, 2
	s_add_u32 s49, s46, 0x80
	s_addc_u32 s5, s47, 0
	s_add_i32 s77, 0, 0x10000
	s_cmp_eq_u32 s72, s4
	s_cselect_b32 s5, s43, s5
	s_cselect_b32 s4, s42, s49
	v_add_u32_e32 v149, s77, v145
	s_cselect_b32 s83, s45, s29
	s_cselect_b32 s82, s44, s27
	s_add_i32 s49, 0, 0x14000
	ds_read_b128 v[140:143], v149
	ds_read_b128 v[150:153], v149 offset:1024
	ds_read_b128 v[154:157], v149 offset:2048
	ds_read_b128 v[158:161], v149 offset:3072
	v_add_u32_e32 v149, s49, v145
	ds_read_b128 v[162:165], v149
	ds_read_b128 v[166:169], v149 offset:1024
	ds_read_b128 v[170:173], v149 offset:2048
	ds_read_b128 v[174:177], v149 offset:3072
	v_lshl_add_u64 v[214:215], s[46:47], 0, v[136:137]
	s_add_i32 m0, s37, 0xc000
	ds_read_b128 v[178:181], v148
	ds_read_b128 v[182:185], v148 offset:1024
	ds_read_b128 v[186:189], v148 offset:2048
	ds_read_b128 v[190:193], v148 offset:3072
	ds_read_b128 v[194:197], v148 offset:4096
	ds_read_b128 v[202:205], v148 offset:5120
	ds_read_b128 v[206:209], v148 offset:6144
	ds_read_b128 v[210:213], v148 offset:7168
	global_load_lds_dwordx4 v[214:215], off
	v_lshl_add_u64 v[214:215], s[46:47], 0, v[138:139]
	s_add_i32 m0, s37, 0xe000
	s_nop 0
	global_load_lds_dwordx4 v[214:215], off
	s_waitcnt lgkmcnt(0)
	s_barrier
	s_setprio 1
	s_waitcnt lgkmcnt(0)
	v_mfma_f32_16x16x32_bf16 v[122:125], v[140:143], v[178:181], 0
	v_mfma_f32_16x16x32_bf16 v[126:129], v[154:157], v[178:181], 0
	v_mfma_f32_16x16x32_bf16 v[110:113], v[140:143], v[186:189], 0
	v_mfma_f32_16x16x32_bf16 v[106:109], v[154:157], v[186:189], 0
	v_mfma_f32_16x16x32_bf16 v[94:97], v[140:143], v[194:197], 0
	v_mfma_f32_16x16x32_bf16 v[90:93], v[154:157], v[194:197], 0
	v_mfma_f32_16x16x32_bf16 v[78:81], v[140:143], v[206:209], 0
	v_mfma_f32_16x16x32_bf16 v[74:77], v[154:157], v[206:209], 0
	v_mfma_f32_16x16x32_bf16 v[122:125], v[150:153], v[182:185], v[122:125]
	v_mfma_f32_16x16x32_bf16 v[126:129], v[158:161], v[182:185], v[126:129]
	v_mfma_f32_16x16x32_bf16 v[110:113], v[150:153], v[190:193], v[110:113]
	v_mfma_f32_16x16x32_bf16 v[106:109], v[158:161], v[190:193], v[106:109]
	v_mfma_f32_16x16x32_bf16 v[94:97], v[150:153], v[202:205], v[94:97]
	v_mfma_f32_16x16x32_bf16 v[90:93], v[158:161], v[202:205], v[90:93]
	v_mfma_f32_16x16x32_bf16 v[78:81], v[150:153], v[210:213], v[78:81]
	v_mfma_f32_16x16x32_bf16 v[74:77], v[158:161], v[210:213], v[74:77]
	s_setprio 0
	s_setprio 1
	v_mfma_f32_16x16x32_bf16 v[118:121], v[162:165], v[178:181], 0
	v_mfma_f32_16x16x32_bf16 v[114:117], v[170:173], v[178:181], 0
	v_mfma_f32_16x16x32_bf16 v[102:105], v[162:165], v[186:189], 0
	v_mfma_f32_16x16x32_bf16 v[98:101], v[170:173], v[186:189], 0
	v_mfma_f32_16x16x32_bf16 v[86:89], v[162:165], v[194:197], 0
	v_mfma_f32_16x16x32_bf16 v[82:85], v[170:173], v[194:197], 0
	v_mfma_f32_16x16x32_bf16 v[70:73], v[162:165], v[206:209], 0
	v_mfma_f32_16x16x32_bf16 v[66:69], v[170:173], v[206:209], 0
	v_mfma_f32_16x16x32_bf16 v[118:121], v[166:169], v[182:185], v[118:121]
	v_mfma_f32_16x16x32_bf16 v[114:117], v[174:177], v[182:185], v[114:117]
	v_mfma_f32_16x16x32_bf16 v[102:105], v[166:169], v[190:193], v[102:105]
	v_mfma_f32_16x16x32_bf16 v[98:101], v[174:177], v[190:193], v[98:101]
	v_mfma_f32_16x16x32_bf16 v[86:89], v[166:169], v[202:205], v[86:89]
	v_mfma_f32_16x16x32_bf16 v[82:85], v[174:177], v[202:205], v[82:85]
	v_mfma_f32_16x16x32_bf16 v[70:73], v[166:169], v[210:213], v[70:73]
	v_mfma_f32_16x16x32_bf16 v[66:69], v[174:177], v[210:213], v[66:69]
	s_setprio 0
	s_barrier
	s_add_i32 s77, s77, s51
	v_lshl_add_u64 v[214:215], s[82:83], 0, v[0:1]
	s_mov_b32 m0, s77
	ds_read_b128 v[178:181], v148 offset:16384
	ds_read_b128 v[182:185], v148 offset:17408
	ds_read_b128 v[186:189], v148 offset:18432
	ds_read_b128 v[190:193], v148 offset:19456
	ds_read_b128 v[194:197], v148 offset:20480
	ds_read_b128 v[202:205], v148 offset:21504
	ds_read_b128 v[206:209], v148 offset:22528
	ds_read_b128 v[210:213], v148 offset:23552
	global_load_lds_dwordx4 v[214:215], off
	s_add_i32 m0, s77, 0x2000
	v_lshl_add_u64 v[216:217], s[82:83], 0, v[130:131]
	s_add_u32 s82, s82, s14
	s_addc_u32 s83, s83, s15
	s_add_i32 s49, s49, s51
	global_load_lds_dwordx4 v[216:217], off
	v_lshl_add_u64 v[218:219], s[82:83], 0, v[0:1]
	s_mov_b32 m0, s49
	v_lshl_add_u64 v[220:221], s[82:83], 0, v[130:131]
	global_load_lds_dwordx4 v[218:219], off
	s_add_i32 m0, s49, 0x2000
	v_lshl_add_u64 v[234:235], s[4:5], 0, v[132:133]
	global_load_lds_dwordx4 v[220:221], off
	s_mov_b32 m0, s37
	v_lshl_add_u64 v[236:237], s[4:5], 0, v[134:135]
	global_load_lds_dwordx4 v[234:235], off
	s_mov_b32 m0, s41
	s_nop 0
	global_load_lds_dwordx4 v[236:237], off
	s_cmp_lg_u32 s76, 1
	s_cbranch_scc1 .Lfw_skip_ip
	s_waitcnt vmcnt(8)
.Lfw_skip_ip:
	s_waitcnt lgkmcnt(0)
	s_barrier
	s_setprio 1
	s_waitcnt lgkmcnt(0)
	v_mfma_f32_16x16x32_bf16 v[62:65], v[140:143], v[178:181], 0
	v_mfma_f32_16x16x32_bf16 v[58:61], v[154:157], v[178:181], 0
	v_mfma_f32_16x16x32_bf16 v[46:49], v[140:143], v[186:189], 0
	v_mfma_f32_16x16x32_bf16 v[42:45], v[154:157], v[186:189], 0
	v_mfma_f32_16x16x32_bf16 v[30:33], v[140:143], v[194:197], 0
	v_mfma_f32_16x16x32_bf16 v[26:29], v[154:157], v[194:197], 0
	v_mfma_f32_16x16x32_bf16 v[14:17], v[140:143], v[206:209], 0
	v_mfma_f32_16x16x32_bf16 v[10:13], v[154:157], v[206:209], 0
	v_mfma_f32_16x16x32_bf16 v[62:65], v[150:153], v[182:185], v[62:65]
	v_mfma_f32_16x16x32_bf16 v[58:61], v[158:161], v[182:185], v[58:61]
	v_mfma_f32_16x16x32_bf16 v[46:49], v[150:153], v[190:193], v[46:49]
	v_mfma_f32_16x16x32_bf16 v[42:45], v[158:161], v[190:193], v[42:45]
	v_mfma_f32_16x16x32_bf16 v[30:33], v[150:153], v[202:205], v[30:33]
	v_mfma_f32_16x16x32_bf16 v[26:29], v[158:161], v[202:205], v[26:29]
	v_mfma_f32_16x16x32_bf16 v[14:17], v[150:153], v[210:213], v[14:17]
	v_mfma_f32_16x16x32_bf16 v[10:13], v[158:161], v[210:213], v[10:13]
	s_setprio 0
	s_setprio 1
	v_mfma_f32_16x16x32_bf16 v[54:57], v[162:165], v[178:181], 0
	v_mfma_f32_16x16x32_bf16 v[50:53], v[170:173], v[178:181], 0
	v_mfma_f32_16x16x32_bf16 v[38:41], v[162:165], v[186:189], 0
	v_mfma_f32_16x16x32_bf16 v[34:37], v[170:173], v[186:189], 0
	v_mfma_f32_16x16x32_bf16 v[22:25], v[162:165], v[194:197], 0
	v_mfma_f32_16x16x32_bf16 v[18:21], v[170:173], v[194:197], 0
	v_mfma_f32_16x16x32_bf16 v[6:9], v[162:165], v[206:209], 0
	v_mfma_f32_16x16x32_bf16 v[2:5], v[170:173], v[206:209], 0
	v_mfma_f32_16x16x32_bf16 v[54:57], v[166:169], v[182:185], v[54:57]
	v_mfma_f32_16x16x32_bf16 v[50:53], v[174:177], v[182:185], v[50:53]
	v_mfma_f32_16x16x32_bf16 v[38:41], v[166:169], v[190:193], v[38:41]
	v_mfma_f32_16x16x32_bf16 v[34:37], v[174:177], v[190:193], v[34:37]
	v_mfma_f32_16x16x32_bf16 v[22:25], v[166:169], v[202:205], v[22:25]
	v_mfma_f32_16x16x32_bf16 v[18:21], v[174:177], v[202:205], v[18:21]
	v_mfma_f32_16x16x32_bf16 v[6:9], v[166:169], v[210:213], v[6:9]
	v_mfma_f32_16x16x32_bf16 v[2:5], v[174:177], v[210:213], v[2:5]
	s_setprio 0
	s_barrier
	s_add_i32 s49, 0, 0x18000
	v_add_u32_e32 v149, s49, v145
	s_add_i32 s77, 0, 0x1c000
	ds_read_b128 v[140:143], v149
	ds_read_b128 v[150:153], v149 offset:1024
	ds_read_b128 v[154:157], v149 offset:2048
	ds_read_b128 v[158:161], v149 offset:3072
	v_add_u32_e32 v149, s77, v145
	ds_read_b128 v[162:165], v149
	ds_read_b128 v[166:169], v149 offset:1024
	ds_read_b128 v[170:173], v149 offset:2048
	ds_read_b128 v[174:177], v149 offset:3072
	s_add_u32 s4, s4, s14
	s_addc_u32 s5, s5, s15
	s_mov_b32 m0, s67
	v_lshl_add_u64 v[238:239], s[4:5], 0, v[132:133]
	ds_read_b128 v[178:181], v148 offset:32768
	ds_read_b128 v[182:185], v148 offset:33792
	ds_read_b128 v[186:189], v148 offset:34816
	ds_read_b128 v[190:193], v148 offset:35840
	ds_read_b128 v[194:197], v148 offset:36864
	ds_read_b128 v[202:205], v148 offset:37888
	ds_read_b128 v[206:209], v148 offset:38912
	ds_read_b128 v[210:213], v148 offset:39936
	global_load_lds_dwordx4 v[238:239], off
	v_lshl_add_u64 v[238:239], s[4:5], 0, v[134:135]
	s_mov_b32 m0, s68
	s_nop 0
	global_load_lds_dwordx4 v[238:239], off
	s_waitcnt vmcnt(8)
	s_waitcnt lgkmcnt(0)
	s_barrier
	s_setprio 1
	s_waitcnt lgkmcnt(0)
	v_mfma_f32_16x16x32_bf16 v[122:125], v[140:143], v[178:181], v[122:125]
	v_mfma_f32_16x16x32_bf16 v[126:129], v[154:157], v[178:181], v[126:129]
	v_mfma_f32_16x16x32_bf16 v[110:113], v[140:143], v[186:189], v[110:113]
	v_mfma_f32_16x16x32_bf16 v[106:109], v[154:157], v[186:189], v[106:109]
	v_mfma_f32_16x16x32_bf16 v[94:97], v[140:143], v[194:197], v[94:97]
	v_mfma_f32_16x16x32_bf16 v[90:93], v[154:157], v[194:197], v[90:93]
	v_mfma_f32_16x16x32_bf16 v[78:81], v[140:143], v[206:209], v[78:81]
	v_mfma_f32_16x16x32_bf16 v[74:77], v[154:157], v[206:209], v[74:77]
	v_mfma_f32_16x16x32_bf16 v[122:125], v[150:153], v[182:185], v[122:125]
	v_mfma_f32_16x16x32_bf16 v[126:129], v[158:161], v[182:185], v[126:129]
	v_mfma_f32_16x16x32_bf16 v[110:113], v[150:153], v[190:193], v[110:113]
	v_mfma_f32_16x16x32_bf16 v[106:109], v[158:161], v[190:193], v[106:109]
	v_mfma_f32_16x16x32_bf16 v[94:97], v[150:153], v[202:205], v[94:97]
	v_mfma_f32_16x16x32_bf16 v[90:93], v[158:161], v[202:205], v[90:93]
	v_mfma_f32_16x16x32_bf16 v[78:81], v[150:153], v[210:213], v[78:81]
	v_mfma_f32_16x16x32_bf16 v[74:77], v[158:161], v[210:213], v[74:77]
	s_setprio 0
	s_setprio 1
	v_mfma_f32_16x16x32_bf16 v[118:121], v[162:165], v[178:181], v[118:121]
	v_mfma_f32_16x16x32_bf16 v[114:117], v[170:173], v[178:181], v[114:117]
	v_mfma_f32_16x16x32_bf16 v[102:105], v[162:165], v[186:189], v[102:105]
	v_mfma_f32_16x16x32_bf16 v[98:101], v[170:173], v[186:189], v[98:101]
	v_mfma_f32_16x16x32_bf16 v[86:89], v[162:165], v[194:197], v[86:89]
	v_mfma_f32_16x16x32_bf16 v[82:85], v[170:173], v[194:197], v[82:85]
	v_mfma_f32_16x16x32_bf16 v[70:73], v[162:165], v[206:209], v[70:73]
	v_mfma_f32_16x16x32_bf16 v[66:69], v[170:173], v[206:209], v[66:69]
	v_mfma_f32_16x16x32_bf16 v[118:121], v[166:169], v[182:185], v[118:121]
	v_mfma_f32_16x16x32_bf16 v[114:117], v[174:177], v[182:185], v[114:117]
	v_mfma_f32_16x16x32_bf16 v[102:105], v[166:169], v[190:193], v[102:105]
	v_mfma_f32_16x16x32_bf16 v[98:101], v[174:177], v[190:193], v[98:101]
	v_mfma_f32_16x16x32_bf16 v[86:89], v[166:169], v[202:205], v[86:89]
	v_mfma_f32_16x16x32_bf16 v[82:85], v[174:177], v[202:205], v[82:85]
	v_mfma_f32_16x16x32_bf16 v[70:73], v[166:169], v[210:213], v[70:73]
	v_mfma_f32_16x16x32_bf16 v[66:69], v[174:177], v[210:213], v[66:69]
	s_setprio 0
	s_barrier
	s_add_i32 s4, s49, s51
	v_lshl_add_u64 v[214:215], v[214:215], 0, s[94:95]
	s_mov_b32 m0, s4
	ds_read_b128 v[178:181], v148 offset:49152
	ds_read_b128 v[182:185], v148 offset:50176
	ds_read_b128 v[186:189], v148 offset:51200
	ds_read_b128 v[190:193], v148 offset:52224
	ds_read_b128 v[194:197], v148 offset:53248
	ds_read_b128 v[202:205], v148 offset:54272
	ds_read_b128 v[206:209], v148 offset:55296
	ds_read_b128 v[210:213], v148 offset:56320
	global_load_lds_dwordx4 v[214:215], off
	v_lshl_add_u64 v[214:215], v[216:217], 0, s[94:95]
	s_add_i32 m0, s4, 0x2000
	s_add_i32 s4, s77, s51
	global_load_lds_dwordx4 v[214:215], off
	v_lshl_add_u64 v[214:215], v[218:219], 0, s[94:95]
	s_mov_b32 m0, s4
	s_nop 0
	global_load_lds_dwordx4 v[214:215], off
	v_lshl_add_u64 v[214:215], v[220:221], 0, s[94:95]
	s_add_i32 m0, s4, 0x2000
	s_nop 0
	global_load_lds_dwordx4 v[214:215], off
	v_lshl_add_u64 v[214:215], v[234:235], 0, s[94:95]
	s_mov_b32 m0, s69
	s_nop 0
	global_load_lds_dwordx4 v[214:215], off
	v_lshl_add_u64 v[214:215], v[236:237], 0, s[94:95]
	s_mov_b32 m0, s70
	s_nop 0
	global_load_lds_dwordx4 v[214:215], off
	s_waitcnt vmcnt(8)
	s_waitcnt lgkmcnt(0)
	s_barrier
	s_setprio 1
	s_waitcnt lgkmcnt(0)
	v_mfma_f32_16x16x32_bf16 v[62:65], v[140:143], v[178:181], v[62:65]
	v_mfma_f32_16x16x32_bf16 v[58:61], v[154:157], v[178:181], v[58:61]
	v_mfma_f32_16x16x32_bf16 v[46:49], v[140:143], v[186:189], v[46:49]
	v_mfma_f32_16x16x32_bf16 v[42:45], v[154:157], v[186:189], v[42:45]
	v_mfma_f32_16x16x32_bf16 v[30:33], v[140:143], v[194:197], v[30:33]
	v_mfma_f32_16x16x32_bf16 v[26:29], v[154:157], v[194:197], v[26:29]
	v_mfma_f32_16x16x32_bf16 v[14:17], v[140:143], v[206:209], v[14:17]
	v_mfma_f32_16x16x32_bf16 v[10:13], v[154:157], v[206:209], v[10:13]
	v_mfma_f32_16x16x32_bf16 v[62:65], v[150:153], v[182:185], v[62:65]
	v_mfma_f32_16x16x32_bf16 v[58:61], v[158:161], v[182:185], v[58:61]
	v_mfma_f32_16x16x32_bf16 v[46:49], v[150:153], v[190:193], v[46:49]
	v_mfma_f32_16x16x32_bf16 v[42:45], v[158:161], v[190:193], v[42:45]
	v_mfma_f32_16x16x32_bf16 v[30:33], v[150:153], v[202:205], v[30:33]
	v_mfma_f32_16x16x32_bf16 v[26:29], v[158:161], v[202:205], v[26:29]
	v_mfma_f32_16x16x32_bf16 v[14:17], v[150:153], v[210:213], v[14:17]
	v_mfma_f32_16x16x32_bf16 v[10:13], v[158:161], v[210:213], v[10:13]
	s_setprio 0
	s_setprio 1
	v_mfma_f32_16x16x32_bf16 v[54:57], v[162:165], v[178:181], v[54:57]
	v_mfma_f32_16x16x32_bf16 v[50:53], v[170:173], v[178:181], v[50:53]
	v_mfma_f32_16x16x32_bf16 v[38:41], v[162:165], v[186:189], v[38:41]
	v_mfma_f32_16x16x32_bf16 v[34:37], v[170:173], v[186:189], v[34:37]
	v_mfma_f32_16x16x32_bf16 v[22:25], v[162:165], v[194:197], v[22:25]
	v_mfma_f32_16x16x32_bf16 v[18:21], v[170:173], v[194:197], v[18:21]
	v_mfma_f32_16x16x32_bf16 v[6:9], v[162:165], v[206:209], v[6:9]
	v_mfma_f32_16x16x32_bf16 v[2:5], v[170:173], v[206:209], v[2:5]
	v_mfma_f32_16x16x32_bf16 v[54:57], v[166:169], v[182:185], v[54:57]
	v_mfma_f32_16x16x32_bf16 v[50:53], v[174:177], v[182:185], v[50:53]
	v_mfma_f32_16x16x32_bf16 v[38:41], v[166:169], v[190:193], v[38:41]
	v_mfma_f32_16x16x32_bf16 v[34:37], v[174:177], v[190:193], v[34:37]
	v_mfma_f32_16x16x32_bf16 v[22:25], v[166:169], v[202:205], v[22:25]
	v_mfma_f32_16x16x32_bf16 v[18:21], v[174:177], v[202:205], v[18:21]
	v_mfma_f32_16x16x32_bf16 v[6:9], v[166:169], v[210:213], v[6:9]
	v_mfma_f32_16x16x32_bf16 v[2:5], v[174:177], v[210:213], v[2:5]
	s_setprio 0
	s_barrier
	s_add_u32 s46, s46, 0x100
	s_addc_u32 s47, s47, 0
	s_add_u32 s27, s27, 0x100
	s_addc_u32 s29, s29, 0
	s_cmp_ge_i32 s48, s71
	s_mov_b32 s4, s48
	s_cbranch_scc1 .LBB0_90

.LBB0_95:
	v_mul_f32_e32 v154, 0xbfb8aa3b, v126
	v_exp_f32_e32 v154, v154
	v_mul_f32_e32 v156, 0xbfb8aa3b, v127
	v_exp_f32_e32 v156, v156
	v_mul_f32_e32 v160, 0xbfb8aa3b, v128
	v_add_f32_e32 v154, 1.0, v154
	v_rcp_f32_e32 v154, v154
	v_exp_f32_e32 v160, v160
	v_mul_f32_e32 v140, 0xbfb8aa3b, v122
	v_mul_f32_e32 v155, 0xbfb8aa3b, v123
	v_fma_f32 v154, v154, s92, 0.5
	v_max_f32_e32 v154, 1.0, v154
	v_cvt_u32_f32_e32 v157, v154
	v_add_f32_e32 v154, 1.0, v156
	v_rcp_f32_e32 v154, v154
	v_exp_f32_e32 v153, v140
	v_exp_f32_e32 v155, v155
	v_mul_f32_e32 v156, 0xbfb8aa3b, v124
	v_fma_f32 v154, v154, s92, 0.5
	v_max_f32_e32 v154, 1.0, v154
	v_cvt_u32_f32_e32 v161, v154
	v_add_f32_e32 v154, 1.0, v160
	v_mul_f32_e32 v160, 0xbfb8aa3b, v125
	v_exp_f32_e32 v156, v156
	v_exp_f32_e32 v160, v160
	v_rcp_f32_e32 v154, v154
	v_add_f32_e32 v153, 1.0, v153
	v_add_f32_e32 v155, 1.0, v155
	v_mul_f32_e32 v162, 0xbfb8aa3b, v129
	v_rcp_f32_e32 v153, v153
	v_rcp_f32_e32 v155, v155
	v_add_f32_e32 v156, 1.0, v156
	v_exp_f32_e32 v162, v162
	v_add_f32_e32 v160, 1.0, v160
	v_rcp_f32_e32 v156, v156
	v_rcp_f32_e32 v160, v160
	v_fma_f32 v154, v154, s92, 0.5
	v_max_f32_e32 v154, 1.0, v154
	v_fma_f32 v153, v153, s92, 0.5
	v_fma_f32 v155, v155, s92, 0.5
	v_cvt_u32_f32_sdwa v163, v154 dst_sel:WORD_1 dst_unused:UNUSED_PAD src0_sel:DWORD
	v_add_f32_e32 v154, 1.0, v162
	v_max_f32_e32 v153, 1.0, v153
	v_max_f32_e32 v155, 1.0, v155
	v_fma_f32 v156, v156, s92, 0.5
	v_rcp_f32_e32 v154, v154
	v_fma_f32 v160, v160, s92, 0.5
	v_cvt_u32_f32_e32 v153, v153
	v_cvt_u32_f32_e32 v155, v155
	v_max_f32_e32 v156, 1.0, v156
	v_max_f32_e32 v160, 1.0, v160
	v_cvt_u32_f32_sdwa v156, v156 dst_sel:WORD_1 dst_unused:UNUSED_PAD src0_sel:DWORD
	v_cvt_u32_f32_sdwa v160, v160 dst_sel:BYTE_3 dst_unused:UNUSED_PAD src0_sel:DWORD
	v_fma_f32 v154, v154, s92, 0.5
	v_max_f32_e32 v154, 1.0, v154
	v_lshl_or_b32 v153, v155, 8, v153
	v_cvt_u32_f32_sdwa v162, v154 dst_sel:BYTE_3 dst_unused:UNUSED_PAD src0_sel:DWORD
	v_or3_b32 v154, v153, v156, v160
	v_mul_f32_e32 v156, 0xbfb8aa3b, v114
	v_exp_f32_e32 v156, v156
	v_mul_f32_e32 v160, 0xbfb8aa3b, v115
	v_exp_f32_e32 v160, v160
	v_lshl_or_b32 v155, v161, 8, v157
	v_add_f32_e32 v156, 1.0, v156
	v_rcp_f32_e32 v156, v156
	v_or3_b32 v155, v155, v163, v162
	v_mul_f32_e32 v162, 0xbfb8aa3b, v116
	v_exp_f32_e32 v162, v162
	v_fma_f32 v156, v156, s92, 0.5
	v_max_f32_e32 v156, 1.0, v156
	v_cvt_u32_f32_e32 v161, v156
	v_add_f32_e32 v156, 1.0, v160
	v_rcp_f32_e32 v156, v156
	v_mul_f32_e32 v153, 0xbfb8aa3b, v118
	v_mul_f32_e32 v157, 0xbfb8aa3b, v119
	v_exp_f32_e32 v153, v153
	v_fma_f32 v156, v156, s92, 0.5
	v_max_f32_e32 v156, 1.0, v156
	v_cvt_u32_f32_e32 v163, v156
	v_add_f32_e32 v156, 1.0, v162
	v_exp_f32_e32 v157, v157
	v_mul_f32_e32 v160, 0xbfb8aa3b, v120
	v_rcp_f32_e32 v156, v156
	v_mul_f32_e32 v162, 0xbfb8aa3b, v121
	v_exp_f32_e32 v160, v160
	v_exp_f32_e32 v162, v162
	v_mul_f32_e32 v164, 0xbfb8aa3b, v117
	v_exp_f32_e32 v164, v164
	v_add_f32_e32 v153, 1.0, v153
	v_add_f32_e32 v157, 1.0, v157
	v_fma_f32 v156, v156, s92, 0.5
	v_rcp_f32_e32 v153, v153
	v_rcp_f32_e32 v157, v157
	v_add_f32_e32 v160, 1.0, v160
	v_max_f32_e32 v156, 1.0, v156
	v_add_f32_e32 v162, 1.0, v162
	v_rcp_f32_e32 v160, v160
	v_rcp_f32_e32 v162, v162
	v_cvt_u32_f32_sdwa v165, v156 dst_sel:WORD_1 dst_unused:UNUSED_PAD src0_sel:DWORD
	v_add_f32_e32 v156, 1.0, v164
	v_rcp_f32_e32 v156, v156
	v_fma_f32 v153, v153, s92, 0.5
	v_fma_f32 v157, v157, s92, 0.5
	v_max_f32_e32 v153, 1.0, v153
	v_max_f32_e32 v157, 1.0, v157
	v_fma_f32 v160, v160, s92, 0.5
	v_fma_f32 v162, v162, s92, 0.5
	v_cvt_u32_f32_e32 v153, v153
	v_cvt_u32_f32_e32 v157, v157
	v_max_f32_e32 v160, 1.0, v160
	v_max_f32_e32 v162, 1.0, v162
	v_fma_f32 v156, v156, s92, 0.5
	v_cvt_u32_f32_sdwa v160, v160 dst_sel:WORD_1 dst_unused:UNUSED_PAD src0_sel:DWORD
	v_cvt_u32_f32_sdwa v162, v162 dst_sel:BYTE_3 dst_unused:UNUSED_PAD src0_sel:DWORD
	v_max_f32_e32 v156, 1.0, v156
	v_cvt_u32_f32_sdwa v164, v156 dst_sel:BYTE_3 dst_unused:UNUSED_PAD src0_sel:DWORD
	v_add_u32_e32 v140, s27, v146
	v_mov_b64_e32 v[142:143], s[20:21]
	v_lshl_or_b32 v153, v157, 8, v153
	v_ashrrev_i32_e32 v141, 31, v140
	v_mad_i64_i32 v[158:159], s[4:5], v149, s79, v[142:143]
	v_or3_b32 v156, v153, v160, v162
	v_lshl_or_b32 v153, v163, 8, v161
	v_mul_f32_e32 v157, 0xbfb8aa3b, v110
	v_exp_f32_e32 v160, v157
	v_or3_b32 v157, v153, v165, v164
	v_lshl_add_u64 v[158:159], v[158:159], 0, v[140:141]
	global_store_dwordx4 v[158:159], v[154:157], off
	v_add_f32_e32 v153, 1.0, v160
	v_mul_f32_e32 v160, 0xbfb8aa3b, v108
	v_mul_f32_e32 v154, 0xbfb8aa3b, v106
	v_exp_f32_e32 v154, v154
	v_mul_f32_e32 v156, 0xbfb8aa3b, v107
	v_exp_f32_e32 v156, v156
	v_exp_f32_e32 v160, v160
	v_add_f32_e32 v154, 1.0, v154
	v_rcp_f32_e32 v154, v154
	v_mul_f32_e32 v155, 0xbfb8aa3b, v111
	v_exp_f32_e32 v155, v155
	v_mul_f32_e32 v162, 0xbfb8aa3b, v109
	v_fma_f32 v154, v154, s92, 0.5
	v_max_f32_e32 v154, 1.0, v154
	v_cvt_u32_f32_e32 v157, v154
	v_add_f32_e32 v154, 1.0, v156
	v_rcp_f32_e32 v154, v154
	v_mul_f32_e32 v156, 0xbfb8aa3b, v112
	v_exp_f32_e32 v156, v156
	v_add_f32_e32 v155, 1.0, v155
	v_fma_f32 v154, v154, s92, 0.5
	v_max_f32_e32 v154, 1.0, v154
	v_cvt_u32_f32_e32 v161, v154
	v_add_f32_e32 v154, 1.0, v160
	v_mul_f32_e32 v160, 0xbfb8aa3b, v113
	v_exp_f32_e32 v160, v160
	v_rcp_f32_e32 v154, v154
	v_rcp_f32_e32 v153, v153
	v_rcp_f32_e32 v155, v155
	v_add_f32_e32 v156, 1.0, v156
	v_exp_f32_e32 v162, v162
	v_add_f32_e32 v160, 1.0, v160
	v_rcp_f32_e32 v156, v156
	v_rcp_f32_e32 v160, v160
	v_fma_f32 v154, v154, s92, 0.5
	v_max_f32_e32 v154, 1.0, v154
	v_fma_f32 v153, v153, s92, 0.5
	v_fma_f32 v155, v155, s92, 0.5
	v_cvt_u32_f32_sdwa v163, v154 dst_sel:WORD_1 dst_unused:UNUSED_PAD src0_sel:DWORD
	v_add_f32_e32 v154, 1.0, v162
	v_max_f32_e32 v153, 1.0, v153
	v_max_f32_e32 v155, 1.0, v155
	v_fma_f32 v156, v156, s92, 0.5
	v_rcp_f32_e32 v154, v154
	v_fma_f32 v160, v160, s92, 0.5
	v_cvt_u32_f32_e32 v153, v153
	v_cvt_u32_f32_e32 v155, v155
	v_max_f32_e32 v156, 1.0, v156
	v_max_f32_e32 v160, 1.0, v160
	v_cvt_u32_f32_sdwa v156, v156 dst_sel:WORD_1 dst_unused:UNUSED_PAD src0_sel:DWORD
	v_cvt_u32_f32_sdwa v160, v160 dst_sel:BYTE_3 dst_unused:UNUSED_PAD src0_sel:DWORD
	v_fma_f32 v154, v154, s92, 0.5
	v_max_f32_e32 v154, 1.0, v154
	v_lshl_or_b32 v153, v155, 8, v153
	v_cvt_u32_f32_sdwa v162, v154 dst_sel:BYTE_3 dst_unused:UNUSED_PAD src0_sel:DWORD
	v_or3_b32 v154, v153, v156, v160
	v_mul_f32_e32 v156, 0xbfb8aa3b, v98
	v_exp_f32_e32 v156, v156
	v_mul_f32_e32 v160, 0xbfb8aa3b, v99
	v_exp_f32_e32 v160, v160
	v_lshl_or_b32 v155, v161, 8, v157
	v_add_f32_e32 v156, 1.0, v156
	v_rcp_f32_e32 v156, v156
	v_or3_b32 v155, v155, v163, v162
	v_mul_f32_e32 v162, 0xbfb8aa3b, v100
	v_exp_f32_e32 v162, v162
	v_fma_f32 v156, v156, s92, 0.5
	v_max_f32_e32 v156, 1.0, v156
	v_cvt_u32_f32_e32 v161, v156
	v_add_f32_e32 v156, 1.0, v160
	v_rcp_f32_e32 v156, v156
	v_mul_f32_e32 v153, 0xbfb8aa3b, v102
	v_mul_f32_e32 v157, 0xbfb8aa3b, v103
	v_exp_f32_e32 v153, v153
	v_fma_f32 v156, v156, s92, 0.5
	v_max_f32_e32 v156, 1.0, v156
	v_cvt_u32_f32_e32 v163, v156
	v_add_f32_e32 v156, 1.0, v162
	v_exp_f32_e32 v157, v157
	v_mul_f32_e32 v160, 0xbfb8aa3b, v104
	v_rcp_f32_e32 v156, v156
	v_mul_f32_e32 v162, 0xbfb8aa3b, v105
	v_exp_f32_e32 v160, v160
	v_exp_f32_e32 v162, v162
	v_mul_f32_e32 v164, 0xbfb8aa3b, v101
	v_exp_f32_e32 v164, v164
	v_add_f32_e32 v153, 1.0, v153
	v_add_f32_e32 v157, 1.0, v157
	v_fma_f32 v156, v156, s92, 0.5
	v_rcp_f32_e32 v153, v153
	v_rcp_f32_e32 v157, v157
	v_add_f32_e32 v160, 1.0, v160
	v_max_f32_e32 v156, 1.0, v156
	v_add_f32_e32 v162, 1.0, v162
	v_rcp_f32_e32 v160, v160
	v_rcp_f32_e32 v162, v162
	v_cvt_u32_f32_sdwa v165, v156 dst_sel:WORD_1 dst_unused:UNUSED_PAD src0_sel:DWORD
	v_add_f32_e32 v156, 1.0, v164
	v_rcp_f32_e32 v156, v156
	v_fma_f32 v153, v153, s92, 0.5
	v_fma_f32 v157, v157, s92, 0.5
	v_max_f32_e32 v153, 1.0, v153
	v_max_f32_e32 v157, 1.0, v157
	v_fma_f32 v160, v160, s92, 0.5
	v_fma_f32 v162, v162, s92, 0.5
	v_cvt_u32_f32_e32 v153, v153
	v_cvt_u32_f32_e32 v157, v157
	v_max_f32_e32 v160, 1.0, v160
	v_max_f32_e32 v162, 1.0, v162
	v_fma_f32 v156, v156, s92, 0.5
	v_cvt_u32_f32_sdwa v160, v160 dst_sel:WORD_1 dst_unused:UNUSED_PAD src0_sel:DWORD
	v_cvt_u32_f32_sdwa v162, v162 dst_sel:BYTE_3 dst_unused:UNUSED_PAD src0_sel:DWORD
	v_max_f32_e32 v156, 1.0, v156
	v_cvt_u32_f32_sdwa v164, v156 dst_sel:BYTE_3 dst_unused:UNUSED_PAD src0_sel:DWORD
	v_lshl_or_b32 v153, v157, 8, v153
	v_mad_i64_i32 v[158:159], s[4:5], v152, s79, v[142:143]
	v_or3_b32 v156, v153, v160, v162
	v_lshl_or_b32 v153, v163, 8, v161
	v_mul_f32_e32 v157, 0xbfb8aa3b, v94
	v_exp_f32_e32 v160, v157
	v_or3_b32 v157, v153, v165, v164
	v_lshl_add_u64 v[158:159], v[158:159], 0, v[140:141]
	global_store_dwordx4 v[158:159], v[154:157], off
	v_add_f32_e32 v153, 1.0, v160
	v_mul_f32_e32 v160, 0xbfb8aa3b, v92
	v_mul_f32_e32 v154, 0xbfb8aa3b, v90
	v_exp_f32_e32 v154, v154
	v_mul_f32_e32 v156, 0xbfb8aa3b, v91
	v_exp_f32_e32 v156, v156
	v_exp_f32_e32 v160, v160
	v_add_f32_e32 v154, 1.0, v154
	v_rcp_f32_e32 v154, v154
	v_mul_f32_e32 v155, 0xbfb8aa3b, v95
	v_exp_f32_e32 v155, v155
	v_mul_f32_e32 v162, 0xbfb8aa3b, v93
	v_fma_f32 v154, v154, s92, 0.5
	v_max_f32_e32 v154, 1.0, v154
	v_cvt_u32_f32_e32 v157, v154
	v_add_f32_e32 v154, 1.0, v156
	v_rcp_f32_e32 v154, v154
	v_mul_f32_e32 v156, 0xbfb8aa3b, v96
	v_exp_f32_e32 v156, v156
	v_add_f32_e32 v155, 1.0, v155
	v_fma_f32 v154, v154, s92, 0.5
	v_max_f32_e32 v154, 1.0, v154
	v_cvt_u32_f32_e32 v161, v154
	v_add_f32_e32 v154, 1.0, v160
	v_mul_f32_e32 v160, 0xbfb8aa3b, v97
	v_exp_f32_e32 v160, v160
	v_rcp_f32_e32 v154, v154
	v_rcp_f32_e32 v153, v153
	v_rcp_f32_e32 v155, v155
	v_add_f32_e32 v156, 1.0, v156
	v_exp_f32_e32 v162, v162
	v_add_f32_e32 v160, 1.0, v160
	v_rcp_f32_e32 v156, v156
	v_rcp_f32_e32 v160, v160
	v_fma_f32 v154, v154, s92, 0.5
	v_max_f32_e32 v154, 1.0, v154
	v_fma_f32 v153, v153, s92, 0.5
	v_fma_f32 v155, v155, s92, 0.5
	v_cvt_u32_f32_sdwa v163, v154 dst_sel:WORD_1 dst_unused:UNUSED_PAD src0_sel:DWORD
	v_add_f32_e32 v154, 1.0, v162
	v_max_f32_e32 v153, 1.0, v153
	v_max_f32_e32 v155, 1.0, v155
	v_fma_f32 v156, v156, s92, 0.5
	v_rcp_f32_e32 v154, v154
	v_fma_f32 v160, v160, s92, 0.5
	v_cvt_u32_f32_e32 v153, v153
	v_cvt_u32_f32_e32 v155, v155
	v_max_f32_e32 v156, 1.0, v156
	v_max_f32_e32 v160, 1.0, v160
	v_cvt_u32_f32_sdwa v156, v156 dst_sel:WORD_1 dst_unused:UNUSED_PAD src0_sel:DWORD
	v_cvt_u32_f32_sdwa v160, v160 dst_sel:BYTE_3 dst_unused:UNUSED_PAD src0_sel:DWORD
	v_fma_f32 v154, v154, s92, 0.5
	v_max_f32_e32 v154, 1.0, v154
	v_lshl_or_b32 v153, v155, 8, v153
	v_cvt_u32_f32_sdwa v162, v154 dst_sel:BYTE_3 dst_unused:UNUSED_PAD src0_sel:DWORD
	v_or3_b32 v154, v153, v156, v160
	v_mul_f32_e32 v156, 0xbfb8aa3b, v82
	v_exp_f32_e32 v156, v156
	v_mul_f32_e32 v160, 0xbfb8aa3b, v83
	v_exp_f32_e32 v160, v160
	v_lshl_or_b32 v155, v161, 8, v157
	v_add_f32_e32 v156, 1.0, v156
	v_rcp_f32_e32 v156, v156
	v_or3_b32 v155, v155, v163, v162
	v_mul_f32_e32 v162, 0xbfb8aa3b, v84
	v_exp_f32_e32 v162, v162
	v_fma_f32 v156, v156, s92, 0.5
	v_max_f32_e32 v156, 1.0, v156
	v_cvt_u32_f32_e32 v161, v156
	v_add_f32_e32 v156, 1.0, v160
	v_rcp_f32_e32 v156, v156
	v_mul_f32_e32 v153, 0xbfb8aa3b, v86
	v_mul_f32_e32 v157, 0xbfb8aa3b, v87
	v_exp_f32_e32 v153, v153
	v_fma_f32 v156, v156, s92, 0.5
	v_max_f32_e32 v156, 1.0, v156
	v_cvt_u32_f32_e32 v163, v156
	v_add_f32_e32 v156, 1.0, v162
	v_exp_f32_e32 v157, v157
	v_mul_f32_e32 v160, 0xbfb8aa3b, v88
	v_rcp_f32_e32 v156, v156
	v_mul_f32_e32 v162, 0xbfb8aa3b, v89
	v_exp_f32_e32 v160, v160
	v_exp_f32_e32 v162, v162
	v_mul_f32_e32 v164, 0xbfb8aa3b, v85
	v_exp_f32_e32 v164, v164
	v_add_f32_e32 v153, 1.0, v153
	v_add_f32_e32 v157, 1.0, v157
	v_fma_f32 v156, v156, s92, 0.5
	v_rcp_f32_e32 v153, v153
	v_rcp_f32_e32 v157, v157
	v_add_f32_e32 v160, 1.0, v160
	v_max_f32_e32 v156, 1.0, v156
	v_add_f32_e32 v162, 1.0, v162
	v_rcp_f32_e32 v160, v160
	v_rcp_f32_e32 v162, v162
	v_cvt_u32_f32_sdwa v165, v156 dst_sel:WORD_1 dst_unused:UNUSED_PAD src0_sel:DWORD
	v_add_f32_e32 v156, 1.0, v164
	v_rcp_f32_e32 v156, v156
	v_fma_f32 v153, v153, s92, 0.5
	v_fma_f32 v157, v157, s92, 0.5
	v_max_f32_e32 v153, 1.0, v153
	v_max_f32_e32 v157, 1.0, v157
	v_fma_f32 v160, v160, s92, 0.5
	v_fma_f32 v162, v162, s92, 0.5
	v_cvt_u32_f32_e32 v153, v153
	v_cvt_u32_f32_e32 v157, v157
	v_max_f32_e32 v160, 1.0, v160
	v_max_f32_e32 v162, 1.0, v162
	v_fma_f32 v156, v156, s92, 0.5
	v_cvt_u32_f32_sdwa v160, v160 dst_sel:WORD_1 dst_unused:UNUSED_PAD src0_sel:DWORD
	v_cvt_u32_f32_sdwa v162, v162 dst_sel:BYTE_3 dst_unused:UNUSED_PAD src0_sel:DWORD
	v_max_f32_e32 v156, 1.0, v156
	v_cvt_u32_f32_sdwa v164, v156 dst_sel:BYTE_3 dst_unused:UNUSED_PAD src0_sel:DWORD
	v_lshl_or_b32 v153, v157, 8, v153
	v_mad_i64_i32 v[158:159], s[4:5], v151, s79, v[142:143]
	v_or3_b32 v156, v153, v160, v162
	v_lshl_or_b32 v153, v163, 8, v161
	v_mul_f32_e32 v157, 0xbfb8aa3b, v78
	v_exp_f32_e32 v160, v157
	v_or3_b32 v157, v153, v165, v164
	v_lshl_add_u64 v[158:159], v[158:159], 0, v[140:141]
	global_store_dwordx4 v[158:159], v[154:157], off
	v_add_f32_e32 v153, 1.0, v160
	v_mul_f32_e32 v160, 0xbfb8aa3b, v76
	v_mul_f32_e32 v154, 0xbfb8aa3b, v74
	v_exp_f32_e32 v154, v154
	v_mul_f32_e32 v156, 0xbfb8aa3b, v75
	v_exp_f32_e32 v156, v156
	v_exp_f32_e32 v160, v160
	v_add_f32_e32 v154, 1.0, v154
	v_rcp_f32_e32 v154, v154
	v_mul_f32_e32 v155, 0xbfb8aa3b, v79
	v_exp_f32_e32 v155, v155
	v_mul_f32_e32 v162, 0xbfb8aa3b, v77
	v_fma_f32 v154, v154, s92, 0.5
	v_max_f32_e32 v154, 1.0, v154
	v_cvt_u32_f32_e32 v157, v154
	v_add_f32_e32 v154, 1.0, v156
	v_rcp_f32_e32 v154, v154
	v_mul_f32_e32 v156, 0xbfb8aa3b, v80
	v_exp_f32_e32 v156, v156
	v_add_f32_e32 v155, 1.0, v155
	v_fma_f32 v154, v154, s92, 0.5
	v_max_f32_e32 v154, 1.0, v154
	v_cvt_u32_f32_e32 v161, v154
	v_add_f32_e32 v154, 1.0, v160
	v_mul_f32_e32 v160, 0xbfb8aa3b, v81
	v_exp_f32_e32 v160, v160
	v_rcp_f32_e32 v154, v154
	v_rcp_f32_e32 v153, v153
	v_rcp_f32_e32 v155, v155
	v_add_f32_e32 v156, 1.0, v156
	v_exp_f32_e32 v162, v162
	v_add_f32_e32 v160, 1.0, v160
	v_rcp_f32_e32 v156, v156
	v_rcp_f32_e32 v160, v160
	v_fma_f32 v154, v154, s92, 0.5
	v_max_f32_e32 v154, 1.0, v154
	v_fma_f32 v153, v153, s92, 0.5
	v_fma_f32 v155, v155, s92, 0.5
	v_cvt_u32_f32_sdwa v163, v154 dst_sel:WORD_1 dst_unused:UNUSED_PAD src0_sel:DWORD
	v_add_f32_e32 v154, 1.0, v162
	v_max_f32_e32 v153, 1.0, v153
	v_max_f32_e32 v155, 1.0, v155
	v_fma_f32 v156, v156, s92, 0.5
	v_rcp_f32_e32 v154, v154
	v_fma_f32 v160, v160, s92, 0.5
	v_cvt_u32_f32_e32 v153, v153
	v_cvt_u32_f32_e32 v155, v155
	v_max_f32_e32 v156, 1.0, v156
	v_max_f32_e32 v160, 1.0, v160
	v_cvt_u32_f32_sdwa v156, v156 dst_sel:WORD_1 dst_unused:UNUSED_PAD src0_sel:DWORD
	v_cvt_u32_f32_sdwa v160, v160 dst_sel:BYTE_3 dst_unused:UNUSED_PAD src0_sel:DWORD
	v_fma_f32 v154, v154, s92, 0.5
	v_max_f32_e32 v154, 1.0, v154
	v_lshl_or_b32 v153, v155, 8, v153
	v_cvt_u32_f32_sdwa v162, v154 dst_sel:BYTE_3 dst_unused:UNUSED_PAD src0_sel:DWORD
	v_or3_b32 v154, v153, v156, v160
	v_mul_f32_e32 v156, 0xbfb8aa3b, v66
	v_exp_f32_e32 v156, v156
	v_mul_f32_e32 v160, 0xbfb8aa3b, v67
	v_exp_f32_e32 v160, v160
	v_lshl_or_b32 v155, v161, 8, v157
	v_add_f32_e32 v156, 1.0, v156
	v_rcp_f32_e32 v156, v156
	v_or3_b32 v155, v155, v163, v162
	v_mul_f32_e32 v162, 0xbfb8aa3b, v68
	v_exp_f32_e32 v162, v162
	v_fma_f32 v156, v156, s92, 0.5
	v_max_f32_e32 v156, 1.0, v156
	v_cvt_u32_f32_e32 v161, v156
	v_add_f32_e32 v156, 1.0, v160
	v_rcp_f32_e32 v156, v156
	v_mul_f32_e32 v153, 0xbfb8aa3b, v70
	v_mul_f32_e32 v157, 0xbfb8aa3b, v71
	v_exp_f32_e32 v153, v153
	v_fma_f32 v156, v156, s92, 0.5
	v_max_f32_e32 v156, 1.0, v156
	v_cvt_u32_f32_e32 v163, v156
	v_add_f32_e32 v156, 1.0, v162
	v_exp_f32_e32 v157, v157
	v_mul_f32_e32 v160, 0xbfb8aa3b, v72
	v_rcp_f32_e32 v156, v156
	v_mul_f32_e32 v162, 0xbfb8aa3b, v73
	v_exp_f32_e32 v160, v160
	v_exp_f32_e32 v162, v162
	v_mul_f32_e32 v164, 0xbfb8aa3b, v69
	v_exp_f32_e32 v164, v164
	v_add_f32_e32 v153, 1.0, v153
	v_add_f32_e32 v157, 1.0, v157
	v_fma_f32 v156, v156, s92, 0.5
	v_rcp_f32_e32 v153, v153
	v_rcp_f32_e32 v157, v157
	v_add_f32_e32 v160, 1.0, v160
	v_max_f32_e32 v156, 1.0, v156
	v_add_f32_e32 v162, 1.0, v162
	v_rcp_f32_e32 v160, v160
	v_rcp_f32_e32 v162, v162
	v_cvt_u32_f32_sdwa v165, v156 dst_sel:WORD_1 dst_unused:UNUSED_PAD src0_sel:DWORD
	v_add_f32_e32 v156, 1.0, v164
	v_rcp_f32_e32 v156, v156
	v_fma_f32 v153, v153, s92, 0.5
	v_fma_f32 v157, v157, s92, 0.5
	v_max_f32_e32 v153, 1.0, v153
	v_max_f32_e32 v157, 1.0, v157
	v_fma_f32 v160, v160, s92, 0.5
	v_fma_f32 v162, v162, s92, 0.5
	v_cvt_u32_f32_e32 v153, v153
	v_cvt_u32_f32_e32 v157, v157
	v_max_f32_e32 v160, 1.0, v160
	v_max_f32_e32 v162, 1.0, v162
	v_fma_f32 v156, v156, s92, 0.5
	v_cvt_u32_f32_sdwa v160, v160 dst_sel:WORD_1 dst_unused:UNUSED_PAD src0_sel:DWORD
	v_cvt_u32_f32_sdwa v162, v162 dst_sel:BYTE_3 dst_unused:UNUSED_PAD src0_sel:DWORD
	v_max_f32_e32 v156, 1.0, v156
	v_cvt_u32_f32_sdwa v164, v156 dst_sel:BYTE_3 dst_unused:UNUSED_PAD src0_sel:DWORD
	v_lshl_or_b32 v153, v157, 8, v153
	v_mad_i64_i32 v[158:159], s[4:5], v150, s79, v[142:143]
	v_or3_b32 v156, v153, v160, v162
	v_lshl_or_b32 v153, v163, 8, v161
	v_or3_b32 v157, v153, v165, v164
	v_lshl_add_u64 v[158:159], v[158:159], 0, v[140:141]
	global_store_dwordx4 v[158:159], v[154:157], off
	v_mul_f32_e32 v160, 0xbfb8aa3b, v60
	v_exp_f32_e32 v160, v160
	v_mul_f32_e32 v155, 0xbfb8aa3b, v58
	v_exp_f32_e32 v155, v155
	v_add_u32_e32 v154, 0x80, v149
	v_mad_i64_i32 v[158:159], s[4:5], v154, s79, v[142:143]
	v_add_f32_e32 v154, 1.0, v155
	v_rcp_f32_e32 v154, v154
	v_mul_f32_e32 v156, 0xbfb8aa3b, v59
	v_exp_f32_e32 v156, v156
	v_mul_f32_e32 v153, 0xbfb8aa3b, v62
	v_fma_f32 v154, v154, s92, 0.5
	v_max_f32_e32 v154, 1.0, v154
	v_cvt_u32_f32_e32 v157, v154
	v_add_f32_e32 v154, 1.0, v156
	v_rcp_f32_e32 v154, v154
	v_mul_f32_e32 v155, 0xbfb8aa3b, v63
	v_exp_f32_e32 v153, v153
	v_exp_f32_e32 v155, v155
	v_fma_f32 v154, v154, s92, 0.5
	v_max_f32_e32 v154, 1.0, v154
	v_mul_f32_e32 v156, 0xbfb8aa3b, v64
	v_cvt_u32_f32_e32 v161, v154
	v_add_f32_e32 v154, 1.0, v160
	v_mul_f32_e32 v160, 0xbfb8aa3b, v65
	v_exp_f32_e32 v156, v156
	v_exp_f32_e32 v160, v160
	v_rcp_f32_e32 v154, v154
	v_add_f32_e32 v153, 1.0, v153
	v_add_f32_e32 v155, 1.0, v155
	v_mul_f32_e32 v162, 0xbfb8aa3b, v61
	v_rcp_f32_e32 v153, v153
	v_rcp_f32_e32 v155, v155
	v_add_f32_e32 v156, 1.0, v156
	v_exp_f32_e32 v162, v162
	v_add_f32_e32 v160, 1.0, v160
	v_rcp_f32_e32 v156, v156
	v_rcp_f32_e32 v160, v160
	v_fma_f32 v154, v154, s92, 0.5
	v_max_f32_e32 v154, 1.0, v154
	v_fma_f32 v153, v153, s92, 0.5
	v_fma_f32 v155, v155, s92, 0.5
	v_cvt_u32_f32_sdwa v163, v154 dst_sel:WORD_1 dst_unused:UNUSED_PAD src0_sel:DWORD
	v_add_f32_e32 v154, 1.0, v162
	v_max_f32_e32 v153, 1.0, v153
	v_max_f32_e32 v155, 1.0, v155
	v_fma_f32 v156, v156, s92, 0.5
	v_rcp_f32_e32 v154, v154
	v_fma_f32 v160, v160, s92, 0.5
	v_cvt_u32_f32_e32 v153, v153
	v_cvt_u32_f32_e32 v155, v155
	v_max_f32_e32 v156, 1.0, v156
	v_max_f32_e32 v160, 1.0, v160
	v_cvt_u32_f32_sdwa v156, v156 dst_sel:WORD_1 dst_unused:UNUSED_PAD src0_sel:DWORD
	v_cvt_u32_f32_sdwa v160, v160 dst_sel:BYTE_3 dst_unused:UNUSED_PAD src0_sel:DWORD
	v_fma_f32 v154, v154, s92, 0.5
	v_max_f32_e32 v154, 1.0, v154
	v_lshl_or_b32 v153, v155, 8, v153
	v_cvt_u32_f32_sdwa v162, v154 dst_sel:BYTE_3 dst_unused:UNUSED_PAD src0_sel:DWORD
	v_or3_b32 v154, v153, v156, v160
	v_mul_f32_e32 v156, 0xbfb8aa3b, v50
	v_exp_f32_e32 v156, v156
	v_mul_f32_e32 v160, 0xbfb8aa3b, v51
	v_exp_f32_e32 v160, v160
	v_lshl_or_b32 v155, v161, 8, v157
	v_add_f32_e32 v156, 1.0, v156
	v_rcp_f32_e32 v156, v156
	v_or3_b32 v155, v155, v163, v162
	v_mul_f32_e32 v162, 0xbfb8aa3b, v52
	v_exp_f32_e32 v162, v162
	v_fma_f32 v156, v156, s92, 0.5
	v_max_f32_e32 v156, 1.0, v156
	v_cvt_u32_f32_e32 v161, v156
	v_add_f32_e32 v156, 1.0, v160
	v_rcp_f32_e32 v156, v156
	v_mul_f32_e32 v153, 0xbfb8aa3b, v54
	v_mul_f32_e32 v157, 0xbfb8aa3b, v55
	v_exp_f32_e32 v153, v153
	v_fma_f32 v156, v156, s92, 0.5
	v_max_f32_e32 v156, 1.0, v156
	v_cvt_u32_f32_e32 v163, v156
	v_add_f32_e32 v156, 1.0, v162
	v_exp_f32_e32 v157, v157
	v_mul_f32_e32 v160, 0xbfb8aa3b, v56
	v_rcp_f32_e32 v156, v156
	v_mul_f32_e32 v162, 0xbfb8aa3b, v57
	v_exp_f32_e32 v160, v160
	v_exp_f32_e32 v162, v162
	v_mul_f32_e32 v164, 0xbfb8aa3b, v53
	v_exp_f32_e32 v164, v164
	v_add_f32_e32 v153, 1.0, v153
	v_add_f32_e32 v157, 1.0, v157
	v_fma_f32 v156, v156, s92, 0.5
	v_rcp_f32_e32 v153, v153
	v_rcp_f32_e32 v157, v157
	v_add_f32_e32 v160, 1.0, v160
	v_max_f32_e32 v156, 1.0, v156
	v_add_f32_e32 v162, 1.0, v162
	v_rcp_f32_e32 v160, v160
	v_rcp_f32_e32 v162, v162
	v_cvt_u32_f32_sdwa v165, v156 dst_sel:WORD_1 dst_unused:UNUSED_PAD src0_sel:DWORD
	v_add_f32_e32 v156, 1.0, v164
	v_rcp_f32_e32 v156, v156
	v_fma_f32 v153, v153, s92, 0.5
	v_fma_f32 v157, v157, s92, 0.5
	v_max_f32_e32 v153, 1.0, v153
	v_max_f32_e32 v157, 1.0, v157
	v_fma_f32 v160, v160, s92, 0.5
	v_fma_f32 v162, v162, s92, 0.5
	v_cvt_u32_f32_e32 v153, v153
	v_cvt_u32_f32_e32 v157, v157
	v_max_f32_e32 v160, 1.0, v160
	v_max_f32_e32 v162, 1.0, v162
	v_fma_f32 v156, v156, s92, 0.5
	v_cvt_u32_f32_sdwa v160, v160 dst_sel:WORD_1 dst_unused:UNUSED_PAD src0_sel:DWORD
	v_cvt_u32_f32_sdwa v162, v162 dst_sel:BYTE_3 dst_unused:UNUSED_PAD src0_sel:DWORD
	v_max_f32_e32 v156, 1.0, v156
	v_cvt_u32_f32_sdwa v164, v156 dst_sel:BYTE_3 dst_unused:UNUSED_PAD src0_sel:DWORD
	v_lshl_or_b32 v153, v157, 8, v153
	v_or3_b32 v156, v153, v160, v162
	v_lshl_or_b32 v153, v163, 8, v161
	v_or3_b32 v157, v153, v165, v164
	v_lshl_add_u64 v[158:159], v[158:159], 0, v[140:141]
	global_store_dwordx4 v[158:159], v[154:157], off
	v_mul_f32_e32 v160, 0xbfb8aa3b, v44
	v_exp_f32_e32 v160, v160
	v_mul_f32_e32 v155, 0xbfb8aa3b, v42
	v_exp_f32_e32 v155, v155
	v_add_u32_e32 v154, 0x90, v149
	v_mad_i64_i32 v[158:159], s[4:5], v154, s79, v[142:143]
	v_add_f32_e32 v154, 1.0, v155
	v_rcp_f32_e32 v154, v154
	v_mul_f32_e32 v156, 0xbfb8aa3b, v43
	v_exp_f32_e32 v156, v156
	v_mul_f32_e32 v153, 0xbfb8aa3b, v46
	v_fma_f32 v154, v154, s92, 0.5
	v_max_f32_e32 v154, 1.0, v154
	v_cvt_u32_f32_e32 v157, v154
	v_add_f32_e32 v154, 1.0, v156
	v_rcp_f32_e32 v154, v154
	v_mul_f32_e32 v155, 0xbfb8aa3b, v47
	v_exp_f32_e32 v153, v153
	v_exp_f32_e32 v155, v155
	v_fma_f32 v154, v154, s92, 0.5
	v_max_f32_e32 v154, 1.0, v154
	v_mul_f32_e32 v156, 0xbfb8aa3b, v48
	v_cvt_u32_f32_e32 v161, v154
	v_add_f32_e32 v154, 1.0, v160
	v_mul_f32_e32 v160, 0xbfb8aa3b, v49
	v_exp_f32_e32 v156, v156
	v_exp_f32_e32 v160, v160
	v_rcp_f32_e32 v154, v154
	v_add_f32_e32 v153, 1.0, v153
	v_add_f32_e32 v155, 1.0, v155
	v_mul_f32_e32 v162, 0xbfb8aa3b, v45
	v_rcp_f32_e32 v153, v153
	v_rcp_f32_e32 v155, v155
	v_add_f32_e32 v156, 1.0, v156
	v_exp_f32_e32 v162, v162
	v_add_f32_e32 v160, 1.0, v160
	v_rcp_f32_e32 v156, v156
	v_rcp_f32_e32 v160, v160
	v_fma_f32 v154, v154, s92, 0.5
	v_max_f32_e32 v154, 1.0, v154
	v_fma_f32 v153, v153, s92, 0.5
	v_fma_f32 v155, v155, s92, 0.5
	v_cvt_u32_f32_sdwa v163, v154 dst_sel:WORD_1 dst_unused:UNUSED_PAD src0_sel:DWORD
	v_add_f32_e32 v154, 1.0, v162
	v_max_f32_e32 v153, 1.0, v153
	v_max_f32_e32 v155, 1.0, v155
	v_fma_f32 v156, v156, s92, 0.5
	v_rcp_f32_e32 v154, v154
	v_fma_f32 v160, v160, s92, 0.5
	v_cvt_u32_f32_e32 v153, v153
	v_cvt_u32_f32_e32 v155, v155
	v_max_f32_e32 v156, 1.0, v156
	v_max_f32_e32 v160, 1.0, v160
	v_cvt_u32_f32_sdwa v156, v156 dst_sel:WORD_1 dst_unused:UNUSED_PAD src0_sel:DWORD
	v_cvt_u32_f32_sdwa v160, v160 dst_sel:BYTE_3 dst_unused:UNUSED_PAD src0_sel:DWORD
	v_fma_f32 v154, v154, s92, 0.5
	v_max_f32_e32 v154, 1.0, v154
	v_lshl_or_b32 v153, v155, 8, v153
	v_cvt_u32_f32_sdwa v162, v154 dst_sel:BYTE_3 dst_unused:UNUSED_PAD src0_sel:DWORD
	v_or3_b32 v154, v153, v156, v160
	v_mul_f32_e32 v156, 0xbfb8aa3b, v34
	v_exp_f32_e32 v156, v156
	v_mul_f32_e32 v160, 0xbfb8aa3b, v35
	v_exp_f32_e32 v160, v160
	v_lshl_or_b32 v155, v161, 8, v157
	v_add_f32_e32 v156, 1.0, v156
	v_rcp_f32_e32 v156, v156
	v_or3_b32 v155, v155, v163, v162
	v_mul_f32_e32 v162, 0xbfb8aa3b, v36
	v_exp_f32_e32 v162, v162
	v_fma_f32 v156, v156, s92, 0.5
	v_max_f32_e32 v156, 1.0, v156
	v_cvt_u32_f32_e32 v161, v156
	v_add_f32_e32 v156, 1.0, v160
	v_rcp_f32_e32 v156, v156
	v_mul_f32_e32 v153, 0xbfb8aa3b, v38
	v_mul_f32_e32 v157, 0xbfb8aa3b, v39
	v_exp_f32_e32 v153, v153
	v_fma_f32 v156, v156, s92, 0.5
	v_max_f32_e32 v156, 1.0, v156
	v_cvt_u32_f32_e32 v163, v156
	v_add_f32_e32 v156, 1.0, v162
	v_exp_f32_e32 v157, v157
	v_mul_f32_e32 v160, 0xbfb8aa3b, v40
	v_rcp_f32_e32 v156, v156
	v_mul_f32_e32 v162, 0xbfb8aa3b, v41
	v_exp_f32_e32 v160, v160
	v_exp_f32_e32 v162, v162
	v_mul_f32_e32 v164, 0xbfb8aa3b, v37
	v_exp_f32_e32 v164, v164
	v_add_f32_e32 v153, 1.0, v153
	v_add_f32_e32 v157, 1.0, v157
	v_fma_f32 v156, v156, s92, 0.5
	v_rcp_f32_e32 v153, v153
	v_rcp_f32_e32 v157, v157
	v_add_f32_e32 v160, 1.0, v160
	v_max_f32_e32 v156, 1.0, v156
	v_add_f32_e32 v162, 1.0, v162
	v_rcp_f32_e32 v160, v160
	v_rcp_f32_e32 v162, v162
	v_cvt_u32_f32_sdwa v165, v156 dst_sel:WORD_1 dst_unused:UNUSED_PAD src0_sel:DWORD
	v_add_f32_e32 v156, 1.0, v164
	v_rcp_f32_e32 v156, v156
	v_fma_f32 v153, v153, s92, 0.5
	v_fma_f32 v157, v157, s92, 0.5
	v_max_f32_e32 v153, 1.0, v153
	v_max_f32_e32 v157, 1.0, v157
	v_fma_f32 v160, v160, s92, 0.5
	v_fma_f32 v162, v162, s92, 0.5
	v_cvt_u32_f32_e32 v153, v153
	v_cvt_u32_f32_e32 v157, v157
	v_max_f32_e32 v160, 1.0, v160
	v_max_f32_e32 v162, 1.0, v162
	v_fma_f32 v156, v156, s92, 0.5
	v_cvt_u32_f32_sdwa v160, v160 dst_sel:WORD_1 dst_unused:UNUSED_PAD src0_sel:DWORD
	v_cvt_u32_f32_sdwa v162, v162 dst_sel:BYTE_3 dst_unused:UNUSED_PAD src0_sel:DWORD
	v_max_f32_e32 v156, 1.0, v156
	v_cvt_u32_f32_sdwa v164, v156 dst_sel:BYTE_3 dst_unused:UNUSED_PAD src0_sel:DWORD
	v_lshl_or_b32 v153, v157, 8, v153
	v_or3_b32 v156, v153, v160, v162
	v_lshl_or_b32 v153, v163, 8, v161
	v_or3_b32 v157, v153, v165, v164
	v_lshl_add_u64 v[158:159], v[158:159], 0, v[140:141]
	global_store_dwordx4 v[158:159], v[154:157], off
	v_mul_f32_e32 v160, 0xbfb8aa3b, v28
	v_exp_f32_e32 v160, v160
	v_mul_f32_e32 v155, 0xbfb8aa3b, v26
	v_exp_f32_e32 v155, v155
	v_add_u32_e32 v154, 0xa0, v149
	v_mad_i64_i32 v[158:159], s[4:5], v154, s79, v[142:143]
	v_add_f32_e32 v154, 1.0, v155
	v_rcp_f32_e32 v154, v154
	v_mul_f32_e32 v156, 0xbfb8aa3b, v27
	v_exp_f32_e32 v156, v156
	v_mul_f32_e32 v153, 0xbfb8aa3b, v30
	v_fma_f32 v154, v154, s92, 0.5
	v_max_f32_e32 v154, 1.0, v154
	v_cvt_u32_f32_e32 v157, v154
	v_add_f32_e32 v154, 1.0, v156
	v_rcp_f32_e32 v154, v154
	v_mul_f32_e32 v155, 0xbfb8aa3b, v31
	v_exp_f32_e32 v153, v153
	v_exp_f32_e32 v155, v155
	v_fma_f32 v154, v154, s92, 0.5
	v_max_f32_e32 v154, 1.0, v154
	v_mul_f32_e32 v156, 0xbfb8aa3b, v32
	v_cvt_u32_f32_e32 v161, v154
	v_add_f32_e32 v154, 1.0, v160
	v_mul_f32_e32 v160, 0xbfb8aa3b, v33
	v_exp_f32_e32 v156, v156
	v_exp_f32_e32 v160, v160
	v_rcp_f32_e32 v154, v154
	v_add_f32_e32 v153, 1.0, v153
	v_add_f32_e32 v155, 1.0, v155
	v_mul_f32_e32 v162, 0xbfb8aa3b, v29
	v_rcp_f32_e32 v153, v153
	v_rcp_f32_e32 v155, v155
	v_add_f32_e32 v156, 1.0, v156
	v_exp_f32_e32 v162, v162
	v_add_f32_e32 v160, 1.0, v160
	v_rcp_f32_e32 v156, v156
	v_rcp_f32_e32 v160, v160
	v_fma_f32 v154, v154, s92, 0.5
	v_max_f32_e32 v154, 1.0, v154
	v_fma_f32 v153, v153, s92, 0.5
	v_fma_f32 v155, v155, s92, 0.5
	v_cvt_u32_f32_sdwa v163, v154 dst_sel:WORD_1 dst_unused:UNUSED_PAD src0_sel:DWORD
	v_add_f32_e32 v154, 1.0, v162
	v_max_f32_e32 v153, 1.0, v153
	v_max_f32_e32 v155, 1.0, v155
	v_fma_f32 v156, v156, s92, 0.5
	v_rcp_f32_e32 v154, v154
	v_fma_f32 v160, v160, s92, 0.5
	v_cvt_u32_f32_e32 v153, v153
	v_cvt_u32_f32_e32 v155, v155
	v_max_f32_e32 v156, 1.0, v156
	v_max_f32_e32 v160, 1.0, v160
	v_cvt_u32_f32_sdwa v156, v156 dst_sel:WORD_1 dst_unused:UNUSED_PAD src0_sel:DWORD
	v_cvt_u32_f32_sdwa v160, v160 dst_sel:BYTE_3 dst_unused:UNUSED_PAD src0_sel:DWORD
	v_fma_f32 v154, v154, s92, 0.5
	v_max_f32_e32 v154, 1.0, v154
	v_lshl_or_b32 v153, v155, 8, v153
	v_cvt_u32_f32_sdwa v162, v154 dst_sel:BYTE_3 dst_unused:UNUSED_PAD src0_sel:DWORD
	v_or3_b32 v154, v153, v156, v160
	v_mul_f32_e32 v156, 0xbfb8aa3b, v18
	v_exp_f32_e32 v156, v156
	v_mul_f32_e32 v160, 0xbfb8aa3b, v19
	v_exp_f32_e32 v160, v160
	v_lshl_or_b32 v155, v161, 8, v157
	v_add_f32_e32 v156, 1.0, v156
	v_rcp_f32_e32 v156, v156
	v_or3_b32 v155, v155, v163, v162
	v_mul_f32_e32 v162, 0xbfb8aa3b, v20
	v_exp_f32_e32 v162, v162
	v_fma_f32 v156, v156, s92, 0.5
	v_max_f32_e32 v156, 1.0, v156
	v_cvt_u32_f32_e32 v161, v156
	v_add_f32_e32 v156, 1.0, v160
	v_rcp_f32_e32 v156, v156
	v_mul_f32_e32 v153, 0xbfb8aa3b, v22
	v_mul_f32_e32 v157, 0xbfb8aa3b, v23
	v_exp_f32_e32 v153, v153
	v_fma_f32 v156, v156, s92, 0.5
	v_max_f32_e32 v156, 1.0, v156
	v_cvt_u32_f32_e32 v163, v156
	v_add_f32_e32 v156, 1.0, v162
	v_exp_f32_e32 v157, v157
	v_mul_f32_e32 v160, 0xbfb8aa3b, v24
	v_rcp_f32_e32 v156, v156
	v_mul_f32_e32 v162, 0xbfb8aa3b, v25
	v_exp_f32_e32 v160, v160
	v_exp_f32_e32 v162, v162
	v_mul_f32_e32 v164, 0xbfb8aa3b, v21
	v_exp_f32_e32 v164, v164
	v_add_f32_e32 v153, 1.0, v153
	v_add_f32_e32 v157, 1.0, v157
	v_fma_f32 v156, v156, s92, 0.5
	v_rcp_f32_e32 v153, v153
	v_rcp_f32_e32 v157, v157
	v_add_f32_e32 v160, 1.0, v160
	v_max_f32_e32 v156, 1.0, v156
	v_add_f32_e32 v162, 1.0, v162
	v_rcp_f32_e32 v160, v160
	v_rcp_f32_e32 v162, v162
	v_cvt_u32_f32_sdwa v165, v156 dst_sel:WORD_1 dst_unused:UNUSED_PAD src0_sel:DWORD
	v_add_f32_e32 v156, 1.0, v164
	v_rcp_f32_e32 v156, v156
	v_fma_f32 v153, v153, s92, 0.5
	v_fma_f32 v157, v157, s92, 0.5
	v_max_f32_e32 v153, 1.0, v153
	v_max_f32_e32 v157, 1.0, v157
	v_fma_f32 v160, v160, s92, 0.5
	v_fma_f32 v162, v162, s92, 0.5
	v_cvt_u32_f32_e32 v153, v153
	v_cvt_u32_f32_e32 v157, v157
	v_max_f32_e32 v160, 1.0, v160
	v_max_f32_e32 v162, 1.0, v162
	v_fma_f32 v156, v156, s92, 0.5
	v_cvt_u32_f32_sdwa v160, v160 dst_sel:WORD_1 dst_unused:UNUSED_PAD src0_sel:DWORD
	v_cvt_u32_f32_sdwa v162, v162 dst_sel:BYTE_3 dst_unused:UNUSED_PAD src0_sel:DWORD
	v_max_f32_e32 v156, 1.0, v156
	v_cvt_u32_f32_sdwa v164, v156 dst_sel:BYTE_3 dst_unused:UNUSED_PAD src0_sel:DWORD
	v_lshl_or_b32 v153, v157, 8, v153
	v_or3_b32 v156, v153, v160, v162
	v_lshl_or_b32 v153, v163, 8, v161
	v_or3_b32 v157, v153, v165, v164
	v_lshl_add_u64 v[158:159], v[158:159], 0, v[140:141]
	global_store_dwordx4 v[158:159], v[154:157], off
	v_mul_f32_e32 v158, 0xbfb8aa3b, v12
	v_exp_f32_e32 v158, v158
	v_mul_f32_e32 v155, 0xbfb8aa3b, v10
	v_exp_f32_e32 v155, v155
	v_add_u32_e32 v154, 0xb0, v149
	v_mad_i64_i32 v[142:143], s[4:5], v154, s79, v[142:143]
	v_add_f32_e32 v154, 1.0, v155
	v_rcp_f32_e32 v154, v154
	v_mul_f32_e32 v156, 0xbfb8aa3b, v11
	v_exp_f32_e32 v156, v156
	v_mul_f32_e32 v153, 0xbfb8aa3b, v14
	v_fma_f32 v154, v154, s92, 0.5
	v_max_f32_e32 v154, 1.0, v154
	v_cvt_u32_f32_e32 v157, v154
	v_add_f32_e32 v154, 1.0, v156
	v_rcp_f32_e32 v154, v154
	v_mul_f32_e32 v155, 0xbfb8aa3b, v15
	v_exp_f32_e32 v153, v153
	v_exp_f32_e32 v155, v155
	v_fma_f32 v154, v154, s92, 0.5
	v_max_f32_e32 v154, 1.0, v154
	v_mul_f32_e32 v156, 0xbfb8aa3b, v16
	v_cvt_u32_f32_e32 v159, v154
	v_add_f32_e32 v154, 1.0, v158
	v_mul_f32_e32 v158, 0xbfb8aa3b, v17
	v_exp_f32_e32 v156, v156
	v_exp_f32_e32 v158, v158
	v_rcp_f32_e32 v154, v154
	v_add_f32_e32 v153, 1.0, v153
	v_add_f32_e32 v155, 1.0, v155
	v_mul_f32_e32 v160, 0xbfb8aa3b, v13
	v_rcp_f32_e32 v153, v153
	v_rcp_f32_e32 v155, v155
	v_add_f32_e32 v156, 1.0, v156
	v_exp_f32_e32 v160, v160
	v_add_f32_e32 v158, 1.0, v158
	v_rcp_f32_e32 v156, v156
	v_rcp_f32_e32 v158, v158
	v_fma_f32 v154, v154, s92, 0.5
	v_max_f32_e32 v154, 1.0, v154
	v_fma_f32 v153, v153, s92, 0.5
	v_fma_f32 v155, v155, s92, 0.5
	v_cvt_u32_f32_sdwa v161, v154 dst_sel:WORD_1 dst_unused:UNUSED_PAD src0_sel:DWORD
	v_add_f32_e32 v154, 1.0, v160
	v_max_f32_e32 v153, 1.0, v153
	v_max_f32_e32 v155, 1.0, v155
	v_fma_f32 v156, v156, s92, 0.5
	v_rcp_f32_e32 v154, v154
	v_fma_f32 v158, v158, s92, 0.5
	v_cvt_u32_f32_e32 v153, v153
	v_cvt_u32_f32_e32 v155, v155
	v_max_f32_e32 v156, 1.0, v156
	v_max_f32_e32 v158, 1.0, v158
	v_cvt_u32_f32_sdwa v156, v156 dst_sel:WORD_1 dst_unused:UNUSED_PAD src0_sel:DWORD
	v_cvt_u32_f32_sdwa v158, v158 dst_sel:BYTE_3 dst_unused:UNUSED_PAD src0_sel:DWORD
	v_fma_f32 v154, v154, s92, 0.5
	v_max_f32_e32 v154, 1.0, v154
	v_lshl_or_b32 v153, v155, 8, v153
	v_cvt_u32_f32_sdwa v160, v154 dst_sel:BYTE_3 dst_unused:UNUSED_PAD src0_sel:DWORD
	v_or3_b32 v154, v153, v156, v158
	v_mul_f32_e32 v156, 0xbfb8aa3b, v2
	v_exp_f32_e32 v156, v156
	v_mul_f32_e32 v158, 0xbfb8aa3b, v3
	v_exp_f32_e32 v158, v158
	v_lshl_or_b32 v155, v159, 8, v157
	v_add_f32_e32 v156, 1.0, v156
	v_rcp_f32_e32 v156, v156
	v_or3_b32 v155, v155, v161, v160
	v_mul_f32_e32 v160, 0xbfb8aa3b, v4
	v_exp_f32_e32 v160, v160
	v_fma_f32 v156, v156, s92, 0.5
	v_max_f32_e32 v156, 1.0, v156
	v_cvt_u32_f32_e32 v159, v156
	v_add_f32_e32 v156, 1.0, v158
	v_rcp_f32_e32 v156, v156
	v_mul_f32_e32 v153, 0xbfb8aa3b, v6
	v_mul_f32_e32 v157, 0xbfb8aa3b, v7
	v_exp_f32_e32 v153, v153
	v_fma_f32 v156, v156, s92, 0.5
	v_max_f32_e32 v156, 1.0, v156
	v_cvt_u32_f32_e32 v161, v156
	v_add_f32_e32 v156, 1.0, v160
	v_exp_f32_e32 v157, v157
	v_mul_f32_e32 v158, 0xbfb8aa3b, v8
	v_rcp_f32_e32 v156, v156
	v_mul_f32_e32 v160, 0xbfb8aa3b, v9
	v_exp_f32_e32 v158, v158
	v_exp_f32_e32 v160, v160
	v_mul_f32_e32 v162, 0xbfb8aa3b, v5
	v_exp_f32_e32 v162, v162
	v_add_f32_e32 v153, 1.0, v153
	v_add_f32_e32 v157, 1.0, v157
	v_fma_f32 v156, v156, s92, 0.5
	v_rcp_f32_e32 v153, v153
	v_rcp_f32_e32 v157, v157
	v_add_f32_e32 v158, 1.0, v158
	v_max_f32_e32 v156, 1.0, v156
	v_add_f32_e32 v160, 1.0, v160
	v_rcp_f32_e32 v158, v158
	v_rcp_f32_e32 v160, v160
	v_cvt_u32_f32_sdwa v163, v156 dst_sel:WORD_1 dst_unused:UNUSED_PAD src0_sel:DWORD
	v_add_f32_e32 v156, 1.0, v162
	v_rcp_f32_e32 v156, v156
	v_fma_f32 v153, v153, s92, 0.5
	v_fma_f32 v157, v157, s92, 0.5
	v_max_f32_e32 v153, 1.0, v153
	v_max_f32_e32 v157, 1.0, v157
	v_fma_f32 v158, v158, s92, 0.5
	v_fma_f32 v160, v160, s92, 0.5
	v_cvt_u32_f32_e32 v153, v153
	v_cvt_u32_f32_e32 v157, v157
	v_max_f32_e32 v158, 1.0, v158
	v_max_f32_e32 v160, 1.0, v160
	v_fma_f32 v156, v156, s92, 0.5
	v_cvt_u32_f32_sdwa v158, v158 dst_sel:WORD_1 dst_unused:UNUSED_PAD src0_sel:DWORD
	v_cvt_u32_f32_sdwa v160, v160 dst_sel:BYTE_3 dst_unused:UNUSED_PAD src0_sel:DWORD
	v_max_f32_e32 v156, 1.0, v156
	v_cvt_u32_f32_sdwa v162, v156 dst_sel:BYTE_3 dst_unused:UNUSED_PAD src0_sel:DWORD
	v_lshl_or_b32 v153, v157, 8, v153
	v_or3_b32 v156, v153, v158, v160
	v_lshl_or_b32 v153, v161, 8, v159
	v_or3_b32 v157, v153, v163, v162
	v_lshl_add_u64 v[140:141], v[142:143], 0, v[140:141]
	global_store_dwordx4 v[140:141], v[154:157], off
	s_waitcnt vmcnt(8)
	s_cbranch_execnz .LBB0_94
.LBB0_96:
	v_add_u32_e32 v140, s27, v147
	v_ashrrev_i32_e32 v141, 31, v140
	v_mov_b64_e32 v[142:143], s[18:19]
	v_cvt_pk_bf16_f32 v70, v70, v71
	v_cvt_pk_bf16_f32 v71, v72, v73
	v_cvt_pk_bf16_f32 v72, v66, v67
	v_add_u32_e32 v66, 0x80, v149
	v_cvt_pk_bf16_f32 v54, v54, v55
	v_cvt_pk_bf16_f32 v55, v56, v57
	v_cvt_pk_bf16_f32 v56, v50, v51
	v_add_u32_e32 v50, 0x90, v149
	v_cvt_pk_bf16_f32 v38, v38, v39
	v_cvt_pk_bf16_f32 v39, v40, v41
	v_cvt_pk_bf16_f32 v40, v34, v35
	v_add_u32_e32 v34, 0xa0, v149
	v_cvt_pk_bf16_f32 v22, v22, v23
	v_cvt_pk_bf16_f32 v23, v24, v25
	v_cvt_pk_bf16_f32 v24, v18, v19
	v_add_u32_e32 v18, 0xb0, v149
	v_mad_i64_i32 v[154:155], s[4:5], v149, s93, v[142:143]
	v_lshlrev_b64 v[140:141], 1, v[140:141]
	v_cvt_pk_bf16_f32 v118, v118, v119
	v_cvt_pk_bf16_f32 v119, v120, v121
	v_cvt_pk_bf16_f32 v120, v114, v115
	v_mad_i64_i32 v[114:115], s[4:5], v152, s93, v[142:143]
	v_cvt_pk_bf16_f32 v102, v102, v103
	v_cvt_pk_bf16_f32 v103, v104, v105
	v_cvt_pk_bf16_f32 v104, v98, v99
	v_mad_i64_i32 v[98:99], s[4:5], v151, s93, v[142:143]
	v_cvt_pk_bf16_f32 v86, v86, v87
	v_cvt_pk_bf16_f32 v87, v88, v89
	v_cvt_pk_bf16_f32 v88, v82, v83
	v_mad_i64_i32 v[82:83], s[4:5], v150, s93, v[142:143]
	v_mad_i64_i32 v[66:67], s[4:5], v66, s93, v[142:143]
	v_mad_i64_i32 v[50:51], s[4:5], v50, s93, v[142:143]
	v_mad_i64_i32 v[34:35], s[4:5], v34, s93, v[142:143]
	v_mad_i64_i32 v[18:19], s[4:5], v18, s93, v[142:143]
	v_lshl_add_u64 v[154:155], v[154:155], 0, v[140:141]
	v_cvt_pk_bf16_f32 v122, v122, v123
	v_cvt_pk_bf16_f32 v123, v124, v125
	v_cvt_pk_bf16_f32 v124, v126, v127
	v_cvt_pk_bf16_f32 v125, v128, v129
	v_cvt_pk_bf16_f32 v121, v116, v117
	v_lshl_add_u64 v[114:115], v[114:115], 0, v[140:141]
	v_cvt_pk_bf16_f32 v110, v110, v111
	v_cvt_pk_bf16_f32 v111, v112, v113
	v_cvt_pk_bf16_f32 v112, v106, v107
	v_cvt_pk_bf16_f32 v113, v108, v109
	v_cvt_pk_bf16_f32 v105, v100, v101
	v_lshl_add_u64 v[98:99], v[98:99], 0, v[140:141]
	v_cvt_pk_bf16_f32 v94, v94, v95
	v_cvt_pk_bf16_f32 v95, v96, v97
	v_cvt_pk_bf16_f32 v96, v90, v91
	v_cvt_pk_bf16_f32 v97, v92, v93
	v_cvt_pk_bf16_f32 v89, v84, v85
	v_lshl_add_u64 v[82:83], v[82:83], 0, v[140:141]
	v_cvt_pk_bf16_f32 v78, v78, v79
	v_cvt_pk_bf16_f32 v79, v80, v81
	v_cvt_pk_bf16_f32 v80, v74, v75
	v_cvt_pk_bf16_f32 v81, v76, v77
	v_cvt_pk_bf16_f32 v73, v68, v69
	v_lshl_add_u64 v[66:67], v[66:67], 0, v[140:141]
	v_cvt_pk_bf16_f32 v62, v62, v63
	v_cvt_pk_bf16_f32 v63, v64, v65
	v_cvt_pk_bf16_f32 v64, v58, v59
	v_cvt_pk_bf16_f32 v65, v60, v61
	v_cvt_pk_bf16_f32 v57, v52, v53
	v_lshl_add_u64 v[50:51], v[50:51], 0, v[140:141]
	v_cvt_pk_bf16_f32 v46, v46, v47
	v_cvt_pk_bf16_f32 v47, v48, v49
	v_cvt_pk_bf16_f32 v48, v42, v43
	v_cvt_pk_bf16_f32 v49, v44, v45
	v_cvt_pk_bf16_f32 v41, v36, v37
	v_lshl_add_u64 v[34:35], v[34:35], 0, v[140:141]
	v_cvt_pk_bf16_f32 v30, v30, v31
	v_cvt_pk_bf16_f32 v31, v32, v33
	v_cvt_pk_bf16_f32 v32, v26, v27
	v_cvt_pk_bf16_f32 v33, v28, v29
	v_cvt_pk_bf16_f32 v25, v20, v21
	v_lshl_add_u64 v[18:19], v[18:19], 0, v[140:141]
	v_cvt_pk_bf16_f32 v14, v14, v15
	v_cvt_pk_bf16_f32 v15, v16, v17
	v_cvt_pk_bf16_f32 v16, v10, v11
	v_cvt_pk_bf16_f32 v17, v12, v13
	v_cvt_pk_bf16_f32 v6, v6, v7
	v_cvt_pk_bf16_f32 v7, v8, v9
	v_cvt_pk_bf16_f32 v8, v2, v3
	v_cvt_pk_bf16_f32 v9, v4, v5
	global_store_dwordx4 v[154:155], v[122:125], off
	global_store_dwordx4 v[154:155], v[118:121], off offset:256
	global_store_dwordx4 v[114:115], v[110:113], off
	global_store_dwordx4 v[114:115], v[102:105], off offset:256
	global_store_dwordx4 v[98:99], v[94:97], off
	global_store_dwordx4 v[98:99], v[86:89], off offset:256
	global_store_dwordx4 v[82:83], v[78:81], off
	global_store_dwordx4 v[82:83], v[70:73], off offset:256
	global_store_dwordx4 v[66:67], v[62:65], off
	global_store_dwordx4 v[66:67], v[54:57], off offset:256
	global_store_dwordx4 v[50:51], v[46:49], off
	global_store_dwordx4 v[50:51], v[38:41], off offset:256
	global_store_dwordx4 v[34:35], v[30:33], off
	global_store_dwordx4 v[34:35], v[22:25], off offset:256
	global_store_dwordx4 v[18:19], v[14:17], off
	global_store_dwordx4 v[18:19], v[6:9], off offset:256
	s_waitcnt vmcnt(16)
	s_and_b64 vcc, exec, s[8:9]
	s_mov_b64 s[4:5], -1
	s_cbranch_vccnz .LBB0_82

.LBB0_113:
	s_andn2_b64 vcc, exec, s[14:15]
	s_cbranch_vccnz .LBB0_116
	s_add_u32 s30, s30, 0x80
	s_addc_u32 s31, s31, 0
	s_add_u32 s19, s34, 0x100
	s_addc_u32 s21, s35, 0
	s_mov_b32 s4, 0
	s_add_i32 s34, s4, 2
	s_add_u32 s35, s30, 0x80
	s_addc_u32 s5, s31, 0
	s_add_i32 s58, 0, 0x10000
	s_cmp_eq_u32 s48, s4
	s_cselect_b32 s5, s27, s5
	s_cselect_b32 s4, s26, s35
	s_cselect_b32 s57, s29, s21
	s_cselect_b32 s56, s28, s19
	s_add_i32 s35, 0, 0x14000
	v_add_u32_e32 v156, s58, v141
	v_add_u32_e32 v172, s35, v141
	ds_read_b128 v[144:147], v156
	ds_read_b128 v[148:151], v156 offset:1024
	ds_read_b128 v[152:155], v156 offset:2048
	ds_read_b128 v[156:159], v156 offset:3072
	ds_read_b128 v[160:163], v172
	ds_read_b128 v[164:167], v172 offset:1024
	ds_read_b128 v[168:171], v172 offset:2048
	ds_read_b128 v[172:175], v172 offset:3072
	v_lshl_add_u64 v[196:197], s[30:31], 0, v[136:137]
	s_add_i32 m0, s3, 0xc000
	ds_read_b128 v[176:179], v143
	ds_read_b128 v[180:183], v143 offset:1024
	ds_read_b128 v[184:187], v143 offset:2048
	ds_read_b128 v[188:191], v143 offset:3072
	ds_read_b128 v[192:195], v143 offset:4096
	ds_read_b128 v[202:205], v143 offset:5120
	ds_read_b128 v[206:209], v143 offset:6144
	ds_read_b128 v[210:213], v143 offset:7168
	global_load_lds_dwordx4 v[196:197], off
	v_lshl_add_u64 v[196:197], s[30:31], 0, v[138:139]
	s_add_i32 m0, s3, 0xe000
	s_nop 0
	global_load_lds_dwordx4 v[196:197], off
	s_waitcnt lgkmcnt(0)
	s_barrier
	s_setprio 1
	s_waitcnt lgkmcnt(0)
	v_mfma_f32_16x16x32_bf16 v[122:125], v[144:147], v[176:179], 0
	v_mfma_f32_16x16x32_bf16 v[126:129], v[152:155], v[176:179], 0
	v_mfma_f32_16x16x32_bf16 v[110:113], v[144:147], v[184:187], 0
	v_mfma_f32_16x16x32_bf16 v[106:109], v[152:155], v[184:187], 0
	v_mfma_f32_16x16x32_bf16 v[94:97], v[144:147], v[192:195], 0
	v_mfma_f32_16x16x32_bf16 v[90:93], v[152:155], v[192:195], 0
	v_mfma_f32_16x16x32_bf16 v[78:81], v[144:147], v[206:209], 0
	v_mfma_f32_16x16x32_bf16 v[74:77], v[152:155], v[206:209], 0
	v_mfma_f32_16x16x32_bf16 v[122:125], v[148:151], v[180:183], v[122:125]
	v_mfma_f32_16x16x32_bf16 v[126:129], v[156:159], v[180:183], v[126:129]
	v_mfma_f32_16x16x32_bf16 v[110:113], v[148:151], v[188:191], v[110:113]
	v_mfma_f32_16x16x32_bf16 v[106:109], v[156:159], v[188:191], v[106:109]
	v_mfma_f32_16x16x32_bf16 v[94:97], v[148:151], v[202:205], v[94:97]
	v_mfma_f32_16x16x32_bf16 v[90:93], v[156:159], v[202:205], v[90:93]
	v_mfma_f32_16x16x32_bf16 v[78:81], v[148:151], v[210:213], v[78:81]
	v_mfma_f32_16x16x32_bf16 v[74:77], v[156:159], v[210:213], v[74:77]
	s_setprio 0
	s_setprio 1
	v_mfma_f32_16x16x32_bf16 v[118:121], v[160:163], v[176:179], 0
	v_mfma_f32_16x16x32_bf16 v[114:117], v[168:171], v[176:179], 0
	v_mfma_f32_16x16x32_bf16 v[102:105], v[160:163], v[184:187], 0
	v_mfma_f32_16x16x32_bf16 v[98:101], v[168:171], v[184:187], 0
	v_mfma_f32_16x16x32_bf16 v[86:89], v[160:163], v[192:195], 0
	v_mfma_f32_16x16x32_bf16 v[82:85], v[168:171], v[192:195], 0
	v_mfma_f32_16x16x32_bf16 v[70:73], v[160:163], v[206:209], 0
	v_mfma_f32_16x16x32_bf16 v[66:69], v[168:171], v[206:209], 0
	v_mfma_f32_16x16x32_bf16 v[118:121], v[164:167], v[180:183], v[118:121]
	v_mfma_f32_16x16x32_bf16 v[114:117], v[172:175], v[180:183], v[114:117]
	v_mfma_f32_16x16x32_bf16 v[102:105], v[164:167], v[188:191], v[102:105]
	v_mfma_f32_16x16x32_bf16 v[98:101], v[172:175], v[188:191], v[98:101]
	v_mfma_f32_16x16x32_bf16 v[86:89], v[164:167], v[202:205], v[86:89]
	v_mfma_f32_16x16x32_bf16 v[82:85], v[172:175], v[202:205], v[82:85]
	v_mfma_f32_16x16x32_bf16 v[70:73], v[164:167], v[210:213], v[70:73]
	v_mfma_f32_16x16x32_bf16 v[66:69], v[172:175], v[210:213], v[66:69]
	s_setprio 0
	s_barrier
	s_add_i32 s58, s58, s51
	v_lshl_add_u64 v[196:197], s[56:57], 0, v[0:1]
	s_mov_b32 m0, s58
	ds_read_b128 v[176:179], v143 offset:16384
	ds_read_b128 v[180:183], v143 offset:17408
	ds_read_b128 v[184:187], v143 offset:18432
	ds_read_b128 v[188:191], v143 offset:19456
	ds_read_b128 v[192:195], v143 offset:20480
	ds_read_b128 v[202:205], v143 offset:21504
	ds_read_b128 v[206:209], v143 offset:22528
	ds_read_b128 v[210:213], v143 offset:23552
	global_load_lds_dwordx4 v[196:197], off
	s_add_i32 m0, s58, 0x2000
	v_lshl_add_u64 v[214:215], s[56:57], 0, v[130:131]
	s_add_u32 s56, s56, s8
	s_addc_u32 s57, s57, s9
	s_add_i32 s35, s35, s51
	global_load_lds_dwordx4 v[214:215], off
	v_lshl_add_u64 v[216:217], s[56:57], 0, v[0:1]
	s_mov_b32 m0, s35
	v_lshl_add_u64 v[218:219], s[56:57], 0, v[130:131]
	global_load_lds_dwordx4 v[216:217], off
	s_add_i32 m0, s35, 0x2000
	v_lshl_add_u64 v[220:221], s[4:5], 0, v[132:133]
	global_load_lds_dwordx4 v[218:219], off
	s_mov_b32 m0, s3
	v_lshl_add_u64 v[234:235], s[4:5], 0, v[134:135]
	global_load_lds_dwordx4 v[220:221], off
	s_mov_b32 m0, s42
	s_nop 0
	global_load_lds_dwordx4 v[234:235], off
	s_cmp_lg_u32 s49, 1
	s_cbranch_scc1 .Lfw_skip_kv
	s_waitcnt vmcnt(8)
.Lfw_skip_kv:
	s_waitcnt lgkmcnt(0)
	s_barrier
	s_setprio 1
	s_waitcnt lgkmcnt(0)
	v_mfma_f32_16x16x32_bf16 v[62:65], v[144:147], v[176:179], 0
	v_mfma_f32_16x16x32_bf16 v[58:61], v[152:155], v[176:179], 0
	v_mfma_f32_16x16x32_bf16 v[46:49], v[144:147], v[184:187], 0
	v_mfma_f32_16x16x32_bf16 v[42:45], v[152:155], v[184:187], 0
	v_mfma_f32_16x16x32_bf16 v[30:33], v[144:147], v[192:195], 0
	v_mfma_f32_16x16x32_bf16 v[26:29], v[152:155], v[192:195], 0
	v_mfma_f32_16x16x32_bf16 v[14:17], v[144:147], v[206:209], 0
	v_mfma_f32_16x16x32_bf16 v[10:13], v[152:155], v[206:209], 0
	v_mfma_f32_16x16x32_bf16 v[62:65], v[148:151], v[180:183], v[62:65]
	v_mfma_f32_16x16x32_bf16 v[58:61], v[156:159], v[180:183], v[58:61]
	v_mfma_f32_16x16x32_bf16 v[46:49], v[148:151], v[188:191], v[46:49]
	v_mfma_f32_16x16x32_bf16 v[42:45], v[156:159], v[188:191], v[42:45]
	v_mfma_f32_16x16x32_bf16 v[30:33], v[148:151], v[202:205], v[30:33]
	v_mfma_f32_16x16x32_bf16 v[26:29], v[156:159], v[202:205], v[26:29]
	v_mfma_f32_16x16x32_bf16 v[14:17], v[148:151], v[210:213], v[14:17]
	v_mfma_f32_16x16x32_bf16 v[10:13], v[156:159], v[210:213], v[10:13]
	s_setprio 0
	s_setprio 1
	v_mfma_f32_16x16x32_bf16 v[54:57], v[160:163], v[176:179], 0
	v_mfma_f32_16x16x32_bf16 v[50:53], v[168:171], v[176:179], 0
	v_mfma_f32_16x16x32_bf16 v[38:41], v[160:163], v[184:187], 0
	v_mfma_f32_16x16x32_bf16 v[34:37], v[168:171], v[184:187], 0
	v_mfma_f32_16x16x32_bf16 v[22:25], v[160:163], v[192:195], 0
	v_mfma_f32_16x16x32_bf16 v[18:21], v[168:171], v[192:195], 0
	v_mfma_f32_16x16x32_bf16 v[6:9], v[160:163], v[206:209], 0
	v_mfma_f32_16x16x32_bf16 v[2:5], v[168:171], v[206:209], 0
	v_mfma_f32_16x16x32_bf16 v[54:57], v[164:167], v[180:183], v[54:57]
	v_mfma_f32_16x16x32_bf16 v[50:53], v[172:175], v[180:183], v[50:53]
	v_mfma_f32_16x16x32_bf16 v[38:41], v[164:167], v[188:191], v[38:41]
	v_mfma_f32_16x16x32_bf16 v[34:37], v[172:175], v[188:191], v[34:37]
	v_mfma_f32_16x16x32_bf16 v[22:25], v[164:167], v[202:205], v[22:25]
	v_mfma_f32_16x16x32_bf16 v[18:21], v[172:175], v[202:205], v[18:21]
	v_mfma_f32_16x16x32_bf16 v[6:9], v[164:167], v[210:213], v[6:9]
	v_mfma_f32_16x16x32_bf16 v[2:5], v[172:175], v[210:213], v[2:5]
	s_setprio 0
	s_barrier
	s_add_i32 s35, 0, 0x18000
	s_add_i32 s56, 0, 0x1c000
	v_add_u32_e32 v156, s35, v141
	v_add_u32_e32 v172, s56, v141
	ds_read_b128 v[144:147], v156
	ds_read_b128 v[148:151], v156 offset:1024
	ds_read_b128 v[152:155], v156 offset:2048
	ds_read_b128 v[156:159], v156 offset:3072
	ds_read_b128 v[160:163], v172
	ds_read_b128 v[164:167], v172 offset:1024
	ds_read_b128 v[168:171], v172 offset:2048
	ds_read_b128 v[172:175], v172 offset:3072
	s_add_u32 s4, s4, s8
	s_addc_u32 s5, s5, s9
	s_mov_b32 m0, s43
	v_lshl_add_u64 v[236:237], s[4:5], 0, v[132:133]
	ds_read_b128 v[176:179], v143 offset:32768
	ds_read_b128 v[180:183], v143 offset:33792
	ds_read_b128 v[184:187], v143 offset:34816
	ds_read_b128 v[188:191], v143 offset:35840
	ds_read_b128 v[192:195], v143 offset:36864
	ds_read_b128 v[202:205], v143 offset:37888
	ds_read_b128 v[206:209], v143 offset:38912
	ds_read_b128 v[210:213], v143 offset:39936
	global_load_lds_dwordx4 v[236:237], off
	v_lshl_add_u64 v[236:237], s[4:5], 0, v[134:135]
	s_mov_b32 m0, s44
	s_nop 0
	global_load_lds_dwordx4 v[236:237], off
	s_waitcnt vmcnt(8)
	s_waitcnt lgkmcnt(0)
	s_barrier
	s_setprio 1
	s_waitcnt lgkmcnt(0)
	v_mfma_f32_16x16x32_bf16 v[122:125], v[144:147], v[176:179], v[122:125]
	v_mfma_f32_16x16x32_bf16 v[126:129], v[152:155], v[176:179], v[126:129]
	v_mfma_f32_16x16x32_bf16 v[110:113], v[144:147], v[184:187], v[110:113]
	v_mfma_f32_16x16x32_bf16 v[106:109], v[152:155], v[184:187], v[106:109]
	v_mfma_f32_16x16x32_bf16 v[94:97], v[144:147], v[192:195], v[94:97]
	v_mfma_f32_16x16x32_bf16 v[90:93], v[152:155], v[192:195], v[90:93]
	v_mfma_f32_16x16x32_bf16 v[78:81], v[144:147], v[206:209], v[78:81]
	v_mfma_f32_16x16x32_bf16 v[74:77], v[152:155], v[206:209], v[74:77]
	v_mfma_f32_16x16x32_bf16 v[122:125], v[148:151], v[180:183], v[122:125]
	v_mfma_f32_16x16x32_bf16 v[126:129], v[156:159], v[180:183], v[126:129]
	v_mfma_f32_16x16x32_bf16 v[110:113], v[148:151], v[188:191], v[110:113]
	v_mfma_f32_16x16x32_bf16 v[106:109], v[156:159], v[188:191], v[106:109]
	v_mfma_f32_16x16x32_bf16 v[94:97], v[148:151], v[202:205], v[94:97]
	v_mfma_f32_16x16x32_bf16 v[90:93], v[156:159], v[202:205], v[90:93]
	v_mfma_f32_16x16x32_bf16 v[78:81], v[148:151], v[210:213], v[78:81]
	v_mfma_f32_16x16x32_bf16 v[74:77], v[156:159], v[210:213], v[74:77]
	s_setprio 0
	s_setprio 1
	v_mfma_f32_16x16x32_bf16 v[118:121], v[160:163], v[176:179], v[118:121]
	v_mfma_f32_16x16x32_bf16 v[114:117], v[168:171], v[176:179], v[114:117]
	v_mfma_f32_16x16x32_bf16 v[102:105], v[160:163], v[184:187], v[102:105]
	v_mfma_f32_16x16x32_bf16 v[98:101], v[168:171], v[184:187], v[98:101]
	v_mfma_f32_16x16x32_bf16 v[86:89], v[160:163], v[192:195], v[86:89]
	v_mfma_f32_16x16x32_bf16 v[82:85], v[168:171], v[192:195], v[82:85]
	v_mfma_f32_16x16x32_bf16 v[70:73], v[160:163], v[206:209], v[70:73]
	v_mfma_f32_16x16x32_bf16 v[66:69], v[168:171], v[206:209], v[66:69]
	v_mfma_f32_16x16x32_bf16 v[118:121], v[164:167], v[180:183], v[118:121]
	v_mfma_f32_16x16x32_bf16 v[114:117], v[172:175], v[180:183], v[114:117]
	v_mfma_f32_16x16x32_bf16 v[102:105], v[164:167], v[188:191], v[102:105]
	v_mfma_f32_16x16x32_bf16 v[98:101], v[172:175], v[188:191], v[98:101]
	v_mfma_f32_16x16x32_bf16 v[86:89], v[164:167], v[202:205], v[86:89]
	v_mfma_f32_16x16x32_bf16 v[82:85], v[172:175], v[202:205], v[82:85]
	v_mfma_f32_16x16x32_bf16 v[70:73], v[164:167], v[210:213], v[70:73]
	v_mfma_f32_16x16x32_bf16 v[66:69], v[172:175], v[210:213], v[66:69]
	s_setprio 0
	s_barrier
	s_add_i32 s4, s35, s51
	v_lshl_add_u64 v[196:197], v[196:197], 0, s[94:95]
	s_mov_b32 m0, s4
	ds_read_b128 v[176:179], v143 offset:49152
	ds_read_b128 v[180:183], v143 offset:50176
	ds_read_b128 v[184:187], v143 offset:51200
	ds_read_b128 v[188:191], v143 offset:52224
	ds_read_b128 v[192:195], v143 offset:53248
	ds_read_b128 v[202:205], v143 offset:54272
	ds_read_b128 v[206:209], v143 offset:55296
	ds_read_b128 v[210:213], v143 offset:56320
	global_load_lds_dwordx4 v[196:197], off
	v_lshl_add_u64 v[196:197], v[214:215], 0, s[94:95]
	s_add_i32 m0, s4, 0x2000
	s_add_i32 s4, s56, s51
	global_load_lds_dwordx4 v[196:197], off
	v_lshl_add_u64 v[196:197], v[216:217], 0, s[94:95]
	s_mov_b32 m0, s4
	s_nop 0
	global_load_lds_dwordx4 v[196:197], off
	v_lshl_add_u64 v[196:197], v[218:219], 0, s[94:95]
	s_add_i32 m0, s4, 0x2000
	s_nop 0
	global_load_lds_dwordx4 v[196:197], off
	v_lshl_add_u64 v[196:197], v[220:221], 0, s[94:95]
	s_mov_b32 m0, s46
	s_nop 0
	global_load_lds_dwordx4 v[196:197], off
	v_lshl_add_u64 v[196:197], v[234:235], 0, s[94:95]
	s_mov_b32 m0, s47
	s_nop 0
	global_load_lds_dwordx4 v[196:197], off
	s_waitcnt vmcnt(8)
	s_waitcnt lgkmcnt(0)
	s_barrier
	s_setprio 1
	s_waitcnt lgkmcnt(0)
	v_mfma_f32_16x16x32_bf16 v[62:65], v[144:147], v[176:179], v[62:65]
	v_mfma_f32_16x16x32_bf16 v[58:61], v[152:155], v[176:179], v[58:61]
	v_mfma_f32_16x16x32_bf16 v[46:49], v[144:147], v[184:187], v[46:49]
	v_mfma_f32_16x16x32_bf16 v[42:45], v[152:155], v[184:187], v[42:45]
	v_mfma_f32_16x16x32_bf16 v[30:33], v[144:147], v[192:195], v[30:33]
	v_mfma_f32_16x16x32_bf16 v[26:29], v[152:155], v[192:195], v[26:29]
	v_mfma_f32_16x16x32_bf16 v[14:17], v[144:147], v[206:209], v[14:17]
	v_mfma_f32_16x16x32_bf16 v[10:13], v[152:155], v[206:209], v[10:13]
	v_mfma_f32_16x16x32_bf16 v[62:65], v[148:151], v[180:183], v[62:65]
	v_mfma_f32_16x16x32_bf16 v[58:61], v[156:159], v[180:183], v[58:61]
	v_mfma_f32_16x16x32_bf16 v[46:49], v[148:151], v[188:191], v[46:49]
	v_mfma_f32_16x16x32_bf16 v[42:45], v[156:159], v[188:191], v[42:45]
	v_mfma_f32_16x16x32_bf16 v[30:33], v[148:151], v[202:205], v[30:33]
	v_mfma_f32_16x16x32_bf16 v[26:29], v[156:159], v[202:205], v[26:29]
	v_mfma_f32_16x16x32_bf16 v[14:17], v[148:151], v[210:213], v[14:17]
	v_mfma_f32_16x16x32_bf16 v[10:13], v[156:159], v[210:213], v[10:13]
	s_setprio 0
	s_setprio 1
	v_mfma_f32_16x16x32_bf16 v[54:57], v[160:163], v[176:179], v[54:57]
	v_mfma_f32_16x16x32_bf16 v[50:53], v[168:171], v[176:179], v[50:53]
	v_mfma_f32_16x16x32_bf16 v[38:41], v[160:163], v[184:187], v[38:41]
	v_mfma_f32_16x16x32_bf16 v[34:37], v[168:171], v[184:187], v[34:37]
	v_mfma_f32_16x16x32_bf16 v[22:25], v[160:163], v[192:195], v[22:25]
	v_mfma_f32_16x16x32_bf16 v[18:21], v[168:171], v[192:195], v[18:21]
	v_mfma_f32_16x16x32_bf16 v[6:9], v[160:163], v[206:209], v[6:9]
	v_mfma_f32_16x16x32_bf16 v[2:5], v[168:171], v[206:209], v[2:5]
	v_mfma_f32_16x16x32_bf16 v[54:57], v[164:167], v[180:183], v[54:57]
	v_mfma_f32_16x16x32_bf16 v[50:53], v[172:175], v[180:183], v[50:53]
	v_mfma_f32_16x16x32_bf16 v[38:41], v[164:167], v[188:191], v[38:41]
	v_mfma_f32_16x16x32_bf16 v[34:37], v[172:175], v[188:191], v[34:37]
	v_mfma_f32_16x16x32_bf16 v[22:25], v[164:167], v[202:205], v[22:25]
	v_mfma_f32_16x16x32_bf16 v[18:21], v[172:175], v[202:205], v[18:21]
	v_mfma_f32_16x16x32_bf16 v[6:9], v[164:167], v[210:213], v[6:9]
	v_mfma_f32_16x16x32_bf16 v[2:5], v[172:175], v[210:213], v[2:5]
	s_setprio 0
	s_barrier
	s_add_u32 s30, s30, 0x100
	s_addc_u32 s31, s31, 0
	s_add_u32 s19, s19, 0x100
	s_addc_u32 s21, s21, 0
	s_cmp_ge_i32 s34, s45
	s_mov_b32 s4, s34
	s_cbranch_scc1 .LBB0_116

.LBB0_118:
	v_lshl_add_u32 v144, s50, 8, v140
	v_lshl_add_u32 v146, s55, 8, v142
	v_ashrrev_i32_e32 v145, 31, v144
	v_ashrrev_i32_e32 v147, 31, v146
	v_lshlrev_b64 v[148:149], 12, v[144:145]
	v_lshl_add_u64 v[148:149], s[10:11], 0, v[148:149]
	v_lshlrev_b64 v[146:147], 1, v[146:147]
	v_lshl_add_u64 v[148:149], v[148:149], 0, v[146:147]
	s_mov_b32 s4, 0x80000
	v_cvt_pk_bf16_f32 v62, v62, v63
	v_cvt_pk_bf16_f32 v63, v64, v65
	v_cvt_pk_bf16_f32 v64, v58, v59
	v_add_co_u32_e32 v58, vcc, s4, v148
	s_mov_b64 s[4:5], 0x90000
	s_nop 0
	v_addc_co_u32_e32 v59, vcc, 0, v149, vcc
	v_cvt_pk_bf16_f32 v54, v54, v55
	v_cvt_pk_bf16_f32 v55, v56, v57
	v_cvt_pk_bf16_f32 v56, v50, v51
	v_lshl_add_u64 v[50:51], v[148:149], 0, s[4:5]
	s_mov_b32 s4, 0x90000
	v_cvt_pk_bf16_f32 v46, v46, v47
	v_cvt_pk_bf16_f32 v47, v48, v49
	v_cvt_pk_bf16_f32 v48, v42, v43
	v_add_co_u32_e32 v42, vcc, s4, v148
	s_mov_b64 s[4:5], 0xa0000
	s_nop 0
	v_addc_co_u32_e32 v43, vcc, 0, v149, vcc
	v_cvt_pk_bf16_f32 v38, v38, v39
	v_cvt_pk_bf16_f32 v39, v40, v41
	v_cvt_pk_bf16_f32 v40, v34, v35
	v_lshl_add_u64 v[34:35], v[148:149], 0, s[4:5]
	s_mov_b32 s4, 0xa0000
	v_cvt_pk_bf16_f32 v118, v118, v119
	v_cvt_pk_bf16_f32 v119, v120, v121
	v_cvt_pk_bf16_f32 v120, v114, v115
	v_or_b32_e32 v114, 16, v144
	v_cvt_pk_bf16_f32 v102, v102, v103
	v_cvt_pk_bf16_f32 v103, v104, v105
	v_cvt_pk_bf16_f32 v104, v98, v99
	v_or_b32_e32 v98, 32, v144
	v_cvt_pk_bf16_f32 v86, v86, v87
	v_cvt_pk_bf16_f32 v87, v88, v89
	v_cvt_pk_bf16_f32 v88, v82, v83
	v_or_b32_e32 v82, 48, v144
	v_cvt_pk_bf16_f32 v30, v30, v31
	v_cvt_pk_bf16_f32 v31, v32, v33
	v_cvt_pk_bf16_f32 v32, v26, v27
	v_add_co_u32_e32 v26, vcc, s4, v148
	s_mov_b64 s[4:5], 0xb0000
	v_ashrrev_i32_e32 v115, 31, v114
	v_ashrrev_i32_e32 v99, 31, v98
	v_ashrrev_i32_e32 v83, 31, v82
	v_addc_co_u32_e32 v27, vcc, 0, v149, vcc
	v_cvt_pk_bf16_f32 v22, v22, v23
	v_cvt_pk_bf16_f32 v23, v24, v25
	v_cvt_pk_bf16_f32 v24, v18, v19
	v_lshl_add_u64 v[18:19], v[148:149], 0, s[4:5]
	s_mov_b32 s4, 0xb0000
	v_lshlrev_b64 v[114:115], 12, v[114:115]
	v_lshlrev_b64 v[98:99], 12, v[98:99]
	v_lshlrev_b64 v[82:83], 12, v[82:83]
	v_cvt_pk_bf16_f32 v14, v14, v15
	v_cvt_pk_bf16_f32 v15, v16, v17
	v_cvt_pk_bf16_f32 v16, v10, v11
	v_add_co_u32_e32 v10, vcc, s4, v148
	v_lshl_add_u64 v[114:115], s[10:11], 0, v[114:115]
	v_lshl_add_u64 v[98:99], s[10:11], 0, v[98:99]
	v_lshl_add_u64 v[82:83], s[10:11], 0, v[82:83]
	v_addc_co_u32_e32 v11, vcc, 0, v149, vcc
	v_cvt_pk_bf16_f32 v122, v122, v123
	v_cvt_pk_bf16_f32 v123, v124, v125
	v_cvt_pk_bf16_f32 v124, v126, v127
	v_cvt_pk_bf16_f32 v125, v128, v129
	v_cvt_pk_bf16_f32 v121, v116, v117
	v_lshl_add_u64 v[114:115], v[114:115], 0, v[146:147]
	v_cvt_pk_bf16_f32 v110, v110, v111
	v_cvt_pk_bf16_f32 v111, v112, v113
	v_cvt_pk_bf16_f32 v112, v106, v107
	v_cvt_pk_bf16_f32 v113, v108, v109
	v_cvt_pk_bf16_f32 v105, v100, v101
	v_lshl_add_u64 v[98:99], v[98:99], 0, v[146:147]
	v_cvt_pk_bf16_f32 v94, v94, v95
	v_cvt_pk_bf16_f32 v95, v96, v97
	v_cvt_pk_bf16_f32 v96, v90, v91
	v_cvt_pk_bf16_f32 v97, v92, v93
	v_cvt_pk_bf16_f32 v89, v84, v85
	v_lshl_add_u64 v[82:83], v[82:83], 0, v[146:147]
	v_cvt_pk_bf16_f32 v78, v78, v79
	v_cvt_pk_bf16_f32 v79, v80, v81
	v_cvt_pk_bf16_f32 v80, v74, v75
	v_cvt_pk_bf16_f32 v81, v76, v77
	v_cvt_pk_bf16_f32 v70, v70, v71
	v_cvt_pk_bf16_f32 v71, v72, v73
	v_cvt_pk_bf16_f32 v72, v66, v67
	v_cvt_pk_bf16_f32 v73, v68, v69
	v_lshl_add_u64 v[66:67], v[148:149], 0, s[96:97]
	v_cvt_pk_bf16_f32 v65, v60, v61
	v_cvt_pk_bf16_f32 v57, v52, v53
	v_cvt_pk_bf16_f32 v49, v44, v45
	v_cvt_pk_bf16_f32 v41, v36, v37
	v_cvt_pk_bf16_f32 v33, v28, v29
	v_cvt_pk_bf16_f32 v25, v20, v21
	v_cvt_pk_bf16_f32 v17, v12, v13
	v_cvt_pk_bf16_f32 v6, v6, v7
	v_cvt_pk_bf16_f32 v7, v8, v9
	v_cvt_pk_bf16_f32 v8, v2, v3
	v_cvt_pk_bf16_f32 v9, v4, v5
	s_and_b64 vcc, exec, s[6:7]
	s_mov_b64 s[4:5], -1
	global_store_dwordx4 v[148:149], v[122:125], off
	global_store_dwordx4 v[148:149], v[118:121], off offset:256
	global_store_dwordx4 v[114:115], v[110:113], off
	global_store_dwordx4 v[114:115], v[102:105], off offset:256
	global_store_dwordx4 v[98:99], v[94:97], off
	global_store_dwordx4 v[98:99], v[86:89], off offset:256
	global_store_dwordx4 v[82:83], v[78:81], off
	global_store_dwordx4 v[82:83], v[70:73], off offset:256
	global_store_dwordx4 v[58:59], v[62:65], off
	global_store_dwordx4 v[66:67], v[54:57], off offset:256
	global_store_dwordx4 v[42:43], v[46:49], off
	global_store_dwordx4 v[50:51], v[38:41], off offset:256
	global_store_dwordx4 v[26:27], v[30:33], off
	global_store_dwordx4 v[34:35], v[22:25], off offset:256
	global_store_dwordx4 v[10:11], v[14:17], off
	global_store_dwordx4 v[18:19], v[6:9], off offset:256
	s_waitcnt vmcnt(16)
	s_cbranch_vccnz .LBB0_106
	s_andn2_b64 vcc, exec, s[12:13]
	s_cbranch_vccnz .LBB0_105
	s_barrier
	s_branch .LBB0_105

.LBB0_542:
	s_andn2_b64 vcc, exec, s[14:15]
	s_cbranch_vccnz .LBB0_546
	s_add_u32 s30, s30, 0x80
	s_addc_u32 s31, s31, 0
	s_add_u32 s19, s34, 0x100
	s_addc_u32 s21, s35, 0
	s_mov_b32 s4, 0
	s_add_i32 s34, s4, 2
	s_add_u32 s35, s30, 0x80
	s_addc_u32 s5, s31, 0
	s_add_i32 s51, 0, 0x10000
	s_cmp_eq_u32 s47, s4
	s_cselect_b32 s5, s27, s5
	s_cselect_b32 s4, s26, s35
	s_cselect_b32 s57, s29, s21
	s_cselect_b32 s56, s28, s19
	s_add_i32 s35, 0, 0x14000
	v_add_u32_e32 v156, s51, v141
	v_add_u32_e32 v172, s35, v141
	ds_read_b128 v[144:147], v156
	ds_read_b128 v[148:151], v156 offset:1024
	ds_read_b128 v[152:155], v156 offset:2048
	ds_read_b128 v[156:159], v156 offset:3072
	ds_read_b128 v[160:163], v172
	ds_read_b128 v[164:167], v172 offset:1024
	ds_read_b128 v[168:171], v172 offset:2048
	ds_read_b128 v[172:175], v172 offset:3072
	v_lshl_add_u64 v[196:197], s[30:31], 0, v[136:137]
	s_add_i32 m0, s40, 0xc000
	ds_read_b128 v[176:179], v143
	ds_read_b128 v[180:183], v143 offset:1024
	ds_read_b128 v[184:187], v143 offset:2048
	ds_read_b128 v[188:191], v143 offset:3072
	ds_read_b128 v[192:195], v143 offset:4096
	ds_read_b128 v[202:205], v143 offset:5120
	ds_read_b128 v[206:209], v143 offset:6144
	ds_read_b128 v[210:213], v143 offset:7168
	global_load_lds_dwordx4 v[196:197], off
	v_lshl_add_u64 v[196:197], s[30:31], 0, v[138:139]
	s_add_i32 m0, s40, 0xe000
	s_nop 0
	global_load_lds_dwordx4 v[196:197], off
	s_waitcnt lgkmcnt(0)
	s_barrier
	s_setprio 1
	s_waitcnt lgkmcnt(0)
	v_mfma_f32_16x16x32_bf16 v[122:125], v[144:147], v[176:179], 0
	v_mfma_f32_16x16x32_bf16 v[126:129], v[152:155], v[176:179], 0
	v_mfma_f32_16x16x32_bf16 v[110:113], v[144:147], v[184:187], 0
	v_mfma_f32_16x16x32_bf16 v[106:109], v[152:155], v[184:187], 0
	v_mfma_f32_16x16x32_bf16 v[94:97], v[144:147], v[192:195], 0
	v_mfma_f32_16x16x32_bf16 v[90:93], v[152:155], v[192:195], 0
	v_mfma_f32_16x16x32_bf16 v[78:81], v[144:147], v[206:209], 0
	v_mfma_f32_16x16x32_bf16 v[74:77], v[152:155], v[206:209], 0
	v_mfma_f32_16x16x32_bf16 v[122:125], v[148:151], v[180:183], v[122:125]
	v_mfma_f32_16x16x32_bf16 v[126:129], v[156:159], v[180:183], v[126:129]
	v_mfma_f32_16x16x32_bf16 v[110:113], v[148:151], v[188:191], v[110:113]
	v_mfma_f32_16x16x32_bf16 v[106:109], v[156:159], v[188:191], v[106:109]
	v_mfma_f32_16x16x32_bf16 v[94:97], v[148:151], v[202:205], v[94:97]
	v_mfma_f32_16x16x32_bf16 v[90:93], v[156:159], v[202:205], v[90:93]
	v_mfma_f32_16x16x32_bf16 v[78:81], v[148:151], v[210:213], v[78:81]
	v_mfma_f32_16x16x32_bf16 v[74:77], v[156:159], v[210:213], v[74:77]
	s_setprio 0
	s_setprio 1
	v_mfma_f32_16x16x32_bf16 v[118:121], v[160:163], v[176:179], 0
	v_mfma_f32_16x16x32_bf16 v[114:117], v[168:171], v[176:179], 0
	v_mfma_f32_16x16x32_bf16 v[102:105], v[160:163], v[184:187], 0
	v_mfma_f32_16x16x32_bf16 v[98:101], v[168:171], v[184:187], 0
	v_mfma_f32_16x16x32_bf16 v[86:89], v[160:163], v[192:195], 0
	v_mfma_f32_16x16x32_bf16 v[82:85], v[168:171], v[192:195], 0
	v_mfma_f32_16x16x32_bf16 v[70:73], v[160:163], v[206:209], 0
	v_mfma_f32_16x16x32_bf16 v[66:69], v[168:171], v[206:209], 0
	v_mfma_f32_16x16x32_bf16 v[118:121], v[164:167], v[180:183], v[118:121]
	v_mfma_f32_16x16x32_bf16 v[114:117], v[172:175], v[180:183], v[114:117]
	v_mfma_f32_16x16x32_bf16 v[102:105], v[164:167], v[188:191], v[102:105]
	v_mfma_f32_16x16x32_bf16 v[98:101], v[172:175], v[188:191], v[98:101]
	v_mfma_f32_16x16x32_bf16 v[86:89], v[164:167], v[202:205], v[86:89]
	v_mfma_f32_16x16x32_bf16 v[82:85], v[172:175], v[202:205], v[82:85]
	v_mfma_f32_16x16x32_bf16 v[70:73], v[164:167], v[210:213], v[70:73]
	v_mfma_f32_16x16x32_bf16 v[66:69], v[172:175], v[210:213], v[66:69]
	s_setprio 0
	s_barrier
	s_add_i32 s51, s51, s39
	v_lshl_add_u64 v[196:197], s[56:57], 0, v[0:1]
	s_mov_b32 m0, s51
	ds_read_b128 v[176:179], v143 offset:16384
	ds_read_b128 v[180:183], v143 offset:17408
	ds_read_b128 v[184:187], v143 offset:18432
	ds_read_b128 v[188:191], v143 offset:19456
	ds_read_b128 v[192:195], v143 offset:20480
	ds_read_b128 v[202:205], v143 offset:21504
	ds_read_b128 v[206:209], v143 offset:22528
	ds_read_b128 v[210:213], v143 offset:23552
	global_load_lds_dwordx4 v[196:197], off
	s_add_i32 m0, s51, 0x2000
	v_lshl_add_u64 v[214:215], s[56:57], 0, v[130:131]
	s_add_u32 s56, s56, s8
	s_addc_u32 s57, s57, s9
	s_add_i32 s35, s35, s39
	global_load_lds_dwordx4 v[214:215], off
	v_lshl_add_u64 v[216:217], s[56:57], 0, v[0:1]
	s_mov_b32 m0, s35
	v_lshl_add_u64 v[218:219], s[56:57], 0, v[130:131]
	global_load_lds_dwordx4 v[216:217], off
	s_add_i32 m0, s35, 0x2000
	v_lshl_add_u64 v[220:221], s[4:5], 0, v[132:133]
	global_load_lds_dwordx4 v[218:219], off
	s_mov_b32 m0, s40
	v_lshl_add_u64 v[234:235], s[4:5], 0, v[134:135]
	global_load_lds_dwordx4 v[220:221], off
	s_mov_b32 m0, s41
	s_nop 0
	global_load_lds_dwordx4 v[234:235], off
	s_cmp_lg_u32 s48, 1
	s_cbranch_scc1 .Lfw_skip_wo
	s_waitcnt vmcnt(8)
.Lfw_skip_wo:
	s_waitcnt lgkmcnt(0)
	s_barrier
	s_setprio 1
	s_waitcnt lgkmcnt(0)
	v_mfma_f32_16x16x32_bf16 v[62:65], v[144:147], v[176:179], 0
	v_mfma_f32_16x16x32_bf16 v[58:61], v[152:155], v[176:179], 0
	v_mfma_f32_16x16x32_bf16 v[46:49], v[144:147], v[184:187], 0
	v_mfma_f32_16x16x32_bf16 v[42:45], v[152:155], v[184:187], 0
	v_mfma_f32_16x16x32_bf16 v[30:33], v[144:147], v[192:195], 0
	v_mfma_f32_16x16x32_bf16 v[26:29], v[152:155], v[192:195], 0
	v_mfma_f32_16x16x32_bf16 v[14:17], v[144:147], v[206:209], 0
	v_mfma_f32_16x16x32_bf16 v[10:13], v[152:155], v[206:209], 0
	v_mfma_f32_16x16x32_bf16 v[62:65], v[148:151], v[180:183], v[62:65]
	v_mfma_f32_16x16x32_bf16 v[58:61], v[156:159], v[180:183], v[58:61]
	v_mfma_f32_16x16x32_bf16 v[46:49], v[148:151], v[188:191], v[46:49]
	v_mfma_f32_16x16x32_bf16 v[42:45], v[156:159], v[188:191], v[42:45]
	v_mfma_f32_16x16x32_bf16 v[30:33], v[148:151], v[202:205], v[30:33]
	v_mfma_f32_16x16x32_bf16 v[26:29], v[156:159], v[202:205], v[26:29]
	v_mfma_f32_16x16x32_bf16 v[14:17], v[148:151], v[210:213], v[14:17]
	v_mfma_f32_16x16x32_bf16 v[10:13], v[156:159], v[210:213], v[10:13]
	s_setprio 0
	s_setprio 1
	v_mfma_f32_16x16x32_bf16 v[54:57], v[160:163], v[176:179], 0
	v_mfma_f32_16x16x32_bf16 v[50:53], v[168:171], v[176:179], 0
	v_mfma_f32_16x16x32_bf16 v[38:41], v[160:163], v[184:187], 0
	v_mfma_f32_16x16x32_bf16 v[34:37], v[168:171], v[184:187], 0
	v_mfma_f32_16x16x32_bf16 v[22:25], v[160:163], v[192:195], 0
	v_mfma_f32_16x16x32_bf16 v[18:21], v[168:171], v[192:195], 0
	v_mfma_f32_16x16x32_bf16 v[6:9], v[160:163], v[206:209], 0
	v_mfma_f32_16x16x32_bf16 v[2:5], v[168:171], v[206:209], 0
	v_mfma_f32_16x16x32_bf16 v[54:57], v[164:167], v[180:183], v[54:57]
	v_mfma_f32_16x16x32_bf16 v[50:53], v[172:175], v[180:183], v[50:53]
	v_mfma_f32_16x16x32_bf16 v[38:41], v[164:167], v[188:191], v[38:41]
	v_mfma_f32_16x16x32_bf16 v[34:37], v[172:175], v[188:191], v[34:37]
	v_mfma_f32_16x16x32_bf16 v[22:25], v[164:167], v[202:205], v[22:25]
	v_mfma_f32_16x16x32_bf16 v[18:21], v[172:175], v[202:205], v[18:21]
	v_mfma_f32_16x16x32_bf16 v[6:9], v[164:167], v[210:213], v[6:9]
	v_mfma_f32_16x16x32_bf16 v[2:5], v[172:175], v[210:213], v[2:5]
	s_setprio 0
	s_barrier
	s_add_i32 s35, 0, 0x18000
	s_add_i32 s51, 0, 0x1c000
	v_add_u32_e32 v156, s35, v141
	v_add_u32_e32 v172, s51, v141
	ds_read_b128 v[144:147], v156
	ds_read_b128 v[148:151], v156 offset:1024
	ds_read_b128 v[152:155], v156 offset:2048
	ds_read_b128 v[156:159], v156 offset:3072
	ds_read_b128 v[160:163], v172
	ds_read_b128 v[164:167], v172 offset:1024
	ds_read_b128 v[168:171], v172 offset:2048
	ds_read_b128 v[172:175], v172 offset:3072
	s_add_u32 s4, s4, s8
	s_addc_u32 s5, s5, s9
	s_mov_b32 m0, s42
	v_lshl_add_u64 v[236:237], s[4:5], 0, v[132:133]
	ds_read_b128 v[176:179], v143 offset:32768
	ds_read_b128 v[180:183], v143 offset:33792
	ds_read_b128 v[184:187], v143 offset:34816
	ds_read_b128 v[188:191], v143 offset:35840
	ds_read_b128 v[192:195], v143 offset:36864
	ds_read_b128 v[202:205], v143 offset:37888
	ds_read_b128 v[206:209], v143 offset:38912
	ds_read_b128 v[210:213], v143 offset:39936
	global_load_lds_dwordx4 v[236:237], off
	v_lshl_add_u64 v[236:237], s[4:5], 0, v[134:135]
	s_mov_b32 m0, s43
	s_nop 0
	global_load_lds_dwordx4 v[236:237], off
	s_waitcnt vmcnt(8)
	s_waitcnt lgkmcnt(0)
	s_barrier
	s_setprio 1
	s_waitcnt lgkmcnt(0)
	v_mfma_f32_16x16x32_bf16 v[122:125], v[144:147], v[176:179], v[122:125]
	v_mfma_f32_16x16x32_bf16 v[126:129], v[152:155], v[176:179], v[126:129]
	v_mfma_f32_16x16x32_bf16 v[110:113], v[144:147], v[184:187], v[110:113]
	v_mfma_f32_16x16x32_bf16 v[106:109], v[152:155], v[184:187], v[106:109]
	v_mfma_f32_16x16x32_bf16 v[94:97], v[144:147], v[192:195], v[94:97]
	v_mfma_f32_16x16x32_bf16 v[90:93], v[152:155], v[192:195], v[90:93]
	v_mfma_f32_16x16x32_bf16 v[78:81], v[144:147], v[206:209], v[78:81]
	v_mfma_f32_16x16x32_bf16 v[74:77], v[152:155], v[206:209], v[74:77]
	v_mfma_f32_16x16x32_bf16 v[122:125], v[148:151], v[180:183], v[122:125]
	v_mfma_f32_16x16x32_bf16 v[126:129], v[156:159], v[180:183], v[126:129]
	v_mfma_f32_16x16x32_bf16 v[110:113], v[148:151], v[188:191], v[110:113]
	v_mfma_f32_16x16x32_bf16 v[106:109], v[156:159], v[188:191], v[106:109]
	v_mfma_f32_16x16x32_bf16 v[94:97], v[148:151], v[202:205], v[94:97]
	v_mfma_f32_16x16x32_bf16 v[90:93], v[156:159], v[202:205], v[90:93]
	v_mfma_f32_16x16x32_bf16 v[78:81], v[148:151], v[210:213], v[78:81]
	v_mfma_f32_16x16x32_bf16 v[74:77], v[156:159], v[210:213], v[74:77]
	s_setprio 0
	s_setprio 1
	v_mfma_f32_16x16x32_bf16 v[118:121], v[160:163], v[176:179], v[118:121]
	v_mfma_f32_16x16x32_bf16 v[114:117], v[168:171], v[176:179], v[114:117]
	v_mfma_f32_16x16x32_bf16 v[102:105], v[160:163], v[184:187], v[102:105]
	v_mfma_f32_16x16x32_bf16 v[98:101], v[168:171], v[184:187], v[98:101]
	v_mfma_f32_16x16x32_bf16 v[86:89], v[160:163], v[192:195], v[86:89]
	v_mfma_f32_16x16x32_bf16 v[82:85], v[168:171], v[192:195], v[82:85]
	v_mfma_f32_16x16x32_bf16 v[70:73], v[160:163], v[206:209], v[70:73]
	v_mfma_f32_16x16x32_bf16 v[66:69], v[168:171], v[206:209], v[66:69]
	v_mfma_f32_16x16x32_bf16 v[118:121], v[164:167], v[180:183], v[118:121]
	v_mfma_f32_16x16x32_bf16 v[114:117], v[172:175], v[180:183], v[114:117]
	v_mfma_f32_16x16x32_bf16 v[102:105], v[164:167], v[188:191], v[102:105]
	v_mfma_f32_16x16x32_bf16 v[98:101], v[172:175], v[188:191], v[98:101]
	v_mfma_f32_16x16x32_bf16 v[86:89], v[164:167], v[202:205], v[86:89]
	v_mfma_f32_16x16x32_bf16 v[82:85], v[172:175], v[202:205], v[82:85]
	v_mfma_f32_16x16x32_bf16 v[70:73], v[164:167], v[210:213], v[70:73]
	v_mfma_f32_16x16x32_bf16 v[66:69], v[172:175], v[210:213], v[66:69]
	s_setprio 0
	s_barrier
	s_add_i32 s4, s35, s39
	v_lshl_add_u64 v[196:197], v[196:197], 0, s[94:95]
	s_mov_b32 m0, s4
	ds_read_b128 v[176:179], v143 offset:49152
	ds_read_b128 v[180:183], v143 offset:50176
	ds_read_b128 v[184:187], v143 offset:51200
	ds_read_b128 v[188:191], v143 offset:52224
	ds_read_b128 v[192:195], v143 offset:53248
	ds_read_b128 v[202:205], v143 offset:54272
	ds_read_b128 v[206:209], v143 offset:55296
	ds_read_b128 v[210:213], v143 offset:56320
	global_load_lds_dwordx4 v[196:197], off
	v_lshl_add_u64 v[196:197], v[214:215], 0, s[94:95]
	s_add_i32 m0, s4, 0x2000
	s_add_i32 s4, s51, s39
	global_load_lds_dwordx4 v[196:197], off
	v_lshl_add_u64 v[196:197], v[216:217], 0, s[94:95]
	s_mov_b32 m0, s4
	s_nop 0
	global_load_lds_dwordx4 v[196:197], off
	v_lshl_add_u64 v[196:197], v[218:219], 0, s[94:95]
	s_add_i32 m0, s4, 0x2000
	s_nop 0
	global_load_lds_dwordx4 v[196:197], off
	v_lshl_add_u64 v[196:197], v[220:221], 0, s[94:95]
	s_mov_b32 m0, s45
	s_nop 0
	global_load_lds_dwordx4 v[196:197], off
	v_lshl_add_u64 v[196:197], v[234:235], 0, s[94:95]
	s_mov_b32 m0, s46
	s_nop 0
	global_load_lds_dwordx4 v[196:197], off
	s_waitcnt vmcnt(8)
	s_waitcnt lgkmcnt(0)
	s_barrier
	s_setprio 1
	s_waitcnt lgkmcnt(0)
	v_mfma_f32_16x16x32_bf16 v[62:65], v[144:147], v[176:179], v[62:65]
	v_mfma_f32_16x16x32_bf16 v[58:61], v[152:155], v[176:179], v[58:61]
	v_mfma_f32_16x16x32_bf16 v[46:49], v[144:147], v[184:187], v[46:49]
	v_mfma_f32_16x16x32_bf16 v[42:45], v[152:155], v[184:187], v[42:45]
	v_mfma_f32_16x16x32_bf16 v[30:33], v[144:147], v[192:195], v[30:33]
	v_mfma_f32_16x16x32_bf16 v[26:29], v[152:155], v[192:195], v[26:29]
	v_mfma_f32_16x16x32_bf16 v[14:17], v[144:147], v[206:209], v[14:17]
	v_mfma_f32_16x16x32_bf16 v[10:13], v[152:155], v[206:209], v[10:13]
	v_mfma_f32_16x16x32_bf16 v[62:65], v[148:151], v[180:183], v[62:65]
	v_mfma_f32_16x16x32_bf16 v[58:61], v[156:159], v[180:183], v[58:61]
	v_mfma_f32_16x16x32_bf16 v[46:49], v[148:151], v[188:191], v[46:49]
	v_mfma_f32_16x16x32_bf16 v[42:45], v[156:159], v[188:191], v[42:45]
	v_mfma_f32_16x16x32_bf16 v[30:33], v[148:151], v[202:205], v[30:33]
	v_mfma_f32_16x16x32_bf16 v[26:29], v[156:159], v[202:205], v[26:29]
	v_mfma_f32_16x16x32_bf16 v[14:17], v[148:151], v[210:213], v[14:17]
	v_mfma_f32_16x16x32_bf16 v[10:13], v[156:159], v[210:213], v[10:13]
	s_setprio 0
	s_setprio 1
	v_mfma_f32_16x16x32_bf16 v[54:57], v[160:163], v[176:179], v[54:57]
	v_mfma_f32_16x16x32_bf16 v[50:53], v[168:171], v[176:179], v[50:53]
	v_mfma_f32_16x16x32_bf16 v[38:41], v[160:163], v[184:187], v[38:41]
	v_mfma_f32_16x16x32_bf16 v[34:37], v[168:171], v[184:187], v[34:37]
	v_mfma_f32_16x16x32_bf16 v[22:25], v[160:163], v[192:195], v[22:25]
	v_mfma_f32_16x16x32_bf16 v[18:21], v[168:171], v[192:195], v[18:21]
	v_mfma_f32_16x16x32_bf16 v[6:9], v[160:163], v[206:209], v[6:9]
	v_mfma_f32_16x16x32_bf16 v[2:5], v[168:171], v[206:209], v[2:5]
	v_mfma_f32_16x16x32_bf16 v[54:57], v[164:167], v[180:183], v[54:57]
	v_mfma_f32_16x16x32_bf16 v[50:53], v[172:175], v[180:183], v[50:53]
	v_mfma_f32_16x16x32_bf16 v[38:41], v[164:167], v[188:191], v[38:41]
	v_mfma_f32_16x16x32_bf16 v[34:37], v[172:175], v[188:191], v[34:37]
	v_mfma_f32_16x16x32_bf16 v[22:25], v[164:167], v[202:205], v[22:25]
	v_mfma_f32_16x16x32_bf16 v[18:21], v[172:175], v[202:205], v[18:21]
	v_mfma_f32_16x16x32_bf16 v[6:9], v[164:167], v[210:213], v[6:9]
	v_mfma_f32_16x16x32_bf16 v[2:5], v[172:175], v[210:213], v[2:5]
	s_setprio 0
	s_barrier
	s_add_u32 s30, s30, 0x100
	s_addc_u32 s31, s31, 0
	s_add_u32 s19, s19, 0x100
	s_addc_u32 s21, s21, 0
	s_cmp_ge_i32 s34, s44
	s_mov_b32 s4, s34
	s_cbranch_scc1 .Lpeel_exit_2

.LBB0_548:
	v_lshl_add_u32 v144, s49, 8, v140
	v_lshl_or_b32 v146, s50, 8, v142
	v_ashrrev_i32_e32 v145, 31, v144
	v_ashrrev_i32_e32 v147, 31, v146
	v_lshlrev_b64 v[148:149], 12, v[144:145]
	v_lshl_add_u64 v[148:149], s[12:13], 0, v[148:149]
	v_lshlrev_b64 v[146:147], 1, v[146:147]
	v_lshl_add_u64 v[148:149], v[148:149], 0, v[146:147]
	s_mov_b32 s4, 0x80000
	v_cvt_pk_bf16_f32 v62, v62, v63
	v_cvt_pk_bf16_f32 v63, v64, v65
	v_cvt_pk_bf16_f32 v64, v58, v59
	v_add_co_u32_e32 v58, vcc, s4, v148
	s_mov_b64 s[4:5], 0x90000
	s_nop 0
	v_addc_co_u32_e32 v59, vcc, 0, v149, vcc
	v_cvt_pk_bf16_f32 v54, v54, v55
	v_cvt_pk_bf16_f32 v55, v56, v57
	v_cvt_pk_bf16_f32 v56, v50, v51
	v_lshl_add_u64 v[50:51], v[148:149], 0, s[4:5]
	s_mov_b32 s4, 0x90000
	v_cvt_pk_bf16_f32 v46, v46, v47
	v_cvt_pk_bf16_f32 v47, v48, v49
	v_cvt_pk_bf16_f32 v48, v42, v43
	v_add_co_u32_e32 v42, vcc, s4, v148
	s_mov_b64 s[4:5], 0xa0000
	s_nop 0
	v_addc_co_u32_e32 v43, vcc, 0, v149, vcc
	v_cvt_pk_bf16_f32 v38, v38, v39
	v_cvt_pk_bf16_f32 v39, v40, v41
	v_cvt_pk_bf16_f32 v40, v34, v35
	v_lshl_add_u64 v[34:35], v[148:149], 0, s[4:5]
	s_mov_b32 s4, 0xa0000
	v_cvt_pk_bf16_f32 v118, v118, v119
	v_cvt_pk_bf16_f32 v119, v120, v121
	v_cvt_pk_bf16_f32 v120, v114, v115
	v_or_b32_e32 v114, 16, v144
	v_cvt_pk_bf16_f32 v102, v102, v103
	v_cvt_pk_bf16_f32 v103, v104, v105
	v_cvt_pk_bf16_f32 v104, v98, v99
	v_or_b32_e32 v98, 32, v144
	v_cvt_pk_bf16_f32 v86, v86, v87
	v_cvt_pk_bf16_f32 v87, v88, v89
	v_cvt_pk_bf16_f32 v88, v82, v83
	v_or_b32_e32 v82, 48, v144
	v_cvt_pk_bf16_f32 v30, v30, v31
	v_cvt_pk_bf16_f32 v31, v32, v33
	v_cvt_pk_bf16_f32 v32, v26, v27
	v_add_co_u32_e32 v26, vcc, s4, v148
	s_mov_b64 s[4:5], 0xb0000
	v_ashrrev_i32_e32 v115, 31, v114
	v_ashrrev_i32_e32 v99, 31, v98
	v_ashrrev_i32_e32 v83, 31, v82
	v_addc_co_u32_e32 v27, vcc, 0, v149, vcc
	v_cvt_pk_bf16_f32 v22, v22, v23
	v_cvt_pk_bf16_f32 v23, v24, v25
	v_cvt_pk_bf16_f32 v24, v18, v19
	v_lshl_add_u64 v[18:19], v[148:149], 0, s[4:5]
	s_mov_b32 s4, 0xb0000
	v_lshlrev_b64 v[114:115], 12, v[114:115]
	v_lshlrev_b64 v[98:99], 12, v[98:99]
	v_lshlrev_b64 v[82:83], 12, v[82:83]
	v_cvt_pk_bf16_f32 v14, v14, v15
	v_cvt_pk_bf16_f32 v15, v16, v17
	v_cvt_pk_bf16_f32 v16, v10, v11
	v_add_co_u32_e32 v10, vcc, s4, v148
	v_lshl_add_u64 v[114:115], s[12:13], 0, v[114:115]
	v_lshl_add_u64 v[98:99], s[12:13], 0, v[98:99]
	v_lshl_add_u64 v[82:83], s[12:13], 0, v[82:83]
	v_addc_co_u32_e32 v11, vcc, 0, v149, vcc
	v_cvt_pk_bf16_f32 v122, v122, v123
	v_cvt_pk_bf16_f32 v123, v124, v125
	v_cvt_pk_bf16_f32 v124, v126, v127
	v_cvt_pk_bf16_f32 v125, v128, v129
	v_cvt_pk_bf16_f32 v121, v116, v117
	v_lshl_add_u64 v[114:115], v[114:115], 0, v[146:147]
	v_cvt_pk_bf16_f32 v110, v110, v111
	v_cvt_pk_bf16_f32 v111, v112, v113
	v_cvt_pk_bf16_f32 v112, v106, v107
	v_cvt_pk_bf16_f32 v113, v108, v109
	v_cvt_pk_bf16_f32 v105, v100, v101
	v_lshl_add_u64 v[98:99], v[98:99], 0, v[146:147]
	v_cvt_pk_bf16_f32 v94, v94, v95
	v_cvt_pk_bf16_f32 v95, v96, v97
	v_cvt_pk_bf16_f32 v96, v90, v91
	v_cvt_pk_bf16_f32 v97, v92, v93
	v_cvt_pk_bf16_f32 v89, v84, v85
	v_lshl_add_u64 v[82:83], v[82:83], 0, v[146:147]
	v_cvt_pk_bf16_f32 v78, v78, v79
	v_cvt_pk_bf16_f32 v79, v80, v81
	v_cvt_pk_bf16_f32 v80, v74, v75
	v_cvt_pk_bf16_f32 v81, v76, v77
	v_cvt_pk_bf16_f32 v70, v70, v71
	v_cvt_pk_bf16_f32 v71, v72, v73
	v_cvt_pk_bf16_f32 v72, v66, v67
	v_cvt_pk_bf16_f32 v73, v68, v69
	v_lshl_add_u64 v[66:67], v[148:149], 0, s[96:97]
	v_cvt_pk_bf16_f32 v65, v60, v61
	v_cvt_pk_bf16_f32 v57, v52, v53
	v_cvt_pk_bf16_f32 v49, v44, v45
	v_cvt_pk_bf16_f32 v41, v36, v37
	v_cvt_pk_bf16_f32 v33, v28, v29
	v_cvt_pk_bf16_f32 v25, v20, v21
	v_cvt_pk_bf16_f32 v17, v12, v13
	v_cvt_pk_bf16_f32 v6, v6, v7
	v_cvt_pk_bf16_f32 v7, v8, v9
	v_cvt_pk_bf16_f32 v8, v2, v3
	v_cvt_pk_bf16_f32 v9, v4, v5
	s_and_b64 vcc, exec, s[6:7]
	s_mov_b64 s[4:5], -1
	global_store_dwordx4 v[148:149], v[122:125], off
	global_store_dwordx4 v[148:149], v[118:121], off offset:256
	global_store_dwordx4 v[114:115], v[110:113], off
	global_store_dwordx4 v[114:115], v[102:105], off offset:256
	global_store_dwordx4 v[98:99], v[94:97], off
	global_store_dwordx4 v[98:99], v[86:89], off offset:256
	global_store_dwordx4 v[82:83], v[78:81], off
	global_store_dwordx4 v[82:83], v[70:73], off offset:256
	global_store_dwordx4 v[58:59], v[62:65], off
	global_store_dwordx4 v[66:67], v[54:57], off offset:256
	global_store_dwordx4 v[42:43], v[46:49], off
	global_store_dwordx4 v[50:51], v[38:41], off offset:256
	global_store_dwordx4 v[26:27], v[30:33], off
	global_store_dwordx4 v[34:35], v[22:25], off offset:256
	global_store_dwordx4 v[10:11], v[14:17], off
	global_store_dwordx4 v[18:19], v[6:9], off offset:256
	s_waitcnt vmcnt(16)
	s_cbranch_vccnz .LBB0_535
	s_andn2_b64 vcc, exec, s[10:11]
	s_cbranch_vccnz .LBB0_534
	s_barrier
	s_branch .LBB0_534

.LBB0_838:
	s_andn2_b64 vcc, exec, s[14:15]
	s_cbranch_vccnz .LBB0_841
	s_add_u32 s24, s24, 0x80
	s_addc_u32 s25, s25, 0
	s_add_u32 s26, s26, 0x100
	s_addc_u32 s27, s27, 0
	s_mov_b32 s4, 0
	s_add_i32 s46, s4, 2
	s_add_u32 s47, s24, 0x80
	s_addc_u32 s5, s25, 0
	s_add_i32 s50, 0, 0x10000
	s_cmp_eq_u32 s41, s4
	s_cselect_b32 s5, s21, s5
	s_cselect_b32 s4, s20, s47
	v_add_u32_e32 v145, s50, v142
	s_cselect_b32 s49, s23, s27
	s_cselect_b32 s48, s22, s26
	s_add_i32 s47, 0, 0x14000
	ds_read_b128 v[146:149], v145
	ds_read_b128 v[150:153], v145 offset:1024
	ds_read_b128 v[154:157], v145 offset:2048
	ds_read_b128 v[158:161], v145 offset:3072
	v_add_u32_e32 v145, s47, v142
	ds_read_b128 v[162:165], v145
	ds_read_b128 v[166:169], v145 offset:1024
	ds_read_b128 v[170:173], v145 offset:2048
	ds_read_b128 v[174:177], v145 offset:3072
	v_lshl_add_u64 v[214:215], s[24:25], 0, v[136:137]
	s_add_i32 m0, s34, 0xc000
	ds_read_b128 v[178:181], v144
	ds_read_b128 v[182:185], v144 offset:1024
	ds_read_b128 v[186:189], v144 offset:2048
	ds_read_b128 v[190:193], v144 offset:3072
	ds_read_b128 v[194:197], v144 offset:4096
	ds_read_b128 v[202:205], v144 offset:5120
	ds_read_b128 v[206:209], v144 offset:6144
	ds_read_b128 v[210:213], v144 offset:7168
	global_load_lds_dwordx4 v[214:215], off
	v_lshl_add_u64 v[214:215], s[24:25], 0, v[138:139]
	s_add_i32 m0, s34, 0xe000
	s_nop 0
	global_load_lds_dwordx4 v[214:215], off
	s_waitcnt lgkmcnt(0)
	s_barrier
	s_setprio 1
	s_waitcnt lgkmcnt(0)
	v_mfma_f32_16x16x32_bf16 v[126:129], v[146:149], v[178:181], 0
	v_mfma_f32_16x16x32_bf16 v[122:125], v[154:157], v[178:181], 0
	v_mfma_f32_16x16x32_bf16 v[110:113], v[146:149], v[186:189], 0
	v_mfma_f32_16x16x32_bf16 v[106:109], v[154:157], v[186:189], 0
	v_mfma_f32_16x16x32_bf16 v[94:97], v[146:149], v[194:197], 0
	v_mfma_f32_16x16x32_bf16 v[90:93], v[154:157], v[194:197], 0
	v_mfma_f32_16x16x32_bf16 v[78:81], v[146:149], v[206:209], 0
	v_mfma_f32_16x16x32_bf16 v[74:77], v[154:157], v[206:209], 0
	v_mfma_f32_16x16x32_bf16 v[126:129], v[150:153], v[182:185], v[126:129]
	v_mfma_f32_16x16x32_bf16 v[122:125], v[158:161], v[182:185], v[122:125]
	v_mfma_f32_16x16x32_bf16 v[110:113], v[150:153], v[190:193], v[110:113]
	v_mfma_f32_16x16x32_bf16 v[106:109], v[158:161], v[190:193], v[106:109]
	v_mfma_f32_16x16x32_bf16 v[94:97], v[150:153], v[202:205], v[94:97]
	v_mfma_f32_16x16x32_bf16 v[90:93], v[158:161], v[202:205], v[90:93]
	v_mfma_f32_16x16x32_bf16 v[78:81], v[150:153], v[210:213], v[78:81]
	v_mfma_f32_16x16x32_bf16 v[74:77], v[158:161], v[210:213], v[74:77]
	s_setprio 0
	s_setprio 1
	v_mfma_f32_16x16x32_bf16 v[118:121], v[162:165], v[178:181], 0
	v_mfma_f32_16x16x32_bf16 v[114:117], v[170:173], v[178:181], 0
	v_mfma_f32_16x16x32_bf16 v[102:105], v[162:165], v[186:189], 0
	v_mfma_f32_16x16x32_bf16 v[98:101], v[170:173], v[186:189], 0
	v_mfma_f32_16x16x32_bf16 v[86:89], v[162:165], v[194:197], 0
	v_mfma_f32_16x16x32_bf16 v[82:85], v[170:173], v[194:197], 0
	v_mfma_f32_16x16x32_bf16 v[70:73], v[162:165], v[206:209], 0
	v_mfma_f32_16x16x32_bf16 v[66:69], v[170:173], v[206:209], 0
	v_mfma_f32_16x16x32_bf16 v[118:121], v[166:169], v[182:185], v[118:121]
	v_mfma_f32_16x16x32_bf16 v[114:117], v[174:177], v[182:185], v[114:117]
	v_mfma_f32_16x16x32_bf16 v[102:105], v[166:169], v[190:193], v[102:105]
	v_mfma_f32_16x16x32_bf16 v[98:101], v[174:177], v[190:193], v[98:101]
	v_mfma_f32_16x16x32_bf16 v[86:89], v[166:169], v[202:205], v[86:89]
	v_mfma_f32_16x16x32_bf16 v[82:85], v[174:177], v[202:205], v[82:85]
	v_mfma_f32_16x16x32_bf16 v[70:73], v[166:169], v[210:213], v[70:73]
	v_mfma_f32_16x16x32_bf16 v[66:69], v[174:177], v[210:213], v[66:69]
	s_setprio 0
	s_barrier
	s_add_i32 s50, s50, s31
	v_lshl_add_u64 v[214:215], s[48:49], 0, v[0:1]
	s_mov_b32 m0, s50
	ds_read_b128 v[178:181], v144 offset:16384
	ds_read_b128 v[182:185], v144 offset:17408
	ds_read_b128 v[186:189], v144 offset:18432
	ds_read_b128 v[190:193], v144 offset:19456
	ds_read_b128 v[194:197], v144 offset:20480
	ds_read_b128 v[202:205], v144 offset:21504
	ds_read_b128 v[206:209], v144 offset:22528
	ds_read_b128 v[210:213], v144 offset:23552
	global_load_lds_dwordx4 v[214:215], off
	s_add_i32 m0, s50, 0x2000
	v_lshl_add_u64 v[216:217], s[48:49], 0, v[130:131]
	s_add_u32 s48, s48, s8
	s_addc_u32 s49, s49, s9
	s_add_i32 s47, s47, s31
	global_load_lds_dwordx4 v[216:217], off
	v_lshl_add_u64 v[218:219], s[48:49], 0, v[0:1]
	s_mov_b32 m0, s47
	v_lshl_add_u64 v[220:221], s[48:49], 0, v[130:131]
	global_load_lds_dwordx4 v[218:219], off
	s_add_i32 m0, s47, 0x2000
	v_lshl_add_u64 v[234:235], s[4:5], 0, v[132:133]
	global_load_lds_dwordx4 v[220:221], off
	s_mov_b32 m0, s34
	v_lshl_add_u64 v[236:237], s[4:5], 0, v[134:135]
	global_load_lds_dwordx4 v[234:235], off
	s_mov_b32 m0, s35
	s_nop 0
	global_load_lds_dwordx4 v[236:237], off
	s_cmp_lg_u32 s42, 1
	s_cbranch_scc1 .Lfw_skip_dn
	s_waitcnt vmcnt(8)
.Lfw_skip_dn:
	s_waitcnt lgkmcnt(0)
	s_barrier
	s_setprio 1
	s_waitcnt lgkmcnt(0)
	v_mfma_f32_16x16x32_bf16 v[62:65], v[146:149], v[178:181], 0
	v_mfma_f32_16x16x32_bf16 v[58:61], v[154:157], v[178:181], 0
	v_mfma_f32_16x16x32_bf16 v[46:49], v[146:149], v[186:189], 0
	v_mfma_f32_16x16x32_bf16 v[42:45], v[154:157], v[186:189], 0
	v_mfma_f32_16x16x32_bf16 v[30:33], v[146:149], v[194:197], 0
	v_mfma_f32_16x16x32_bf16 v[26:29], v[154:157], v[194:197], 0
	v_mfma_f32_16x16x32_bf16 v[14:17], v[146:149], v[206:209], 0
	v_mfma_f32_16x16x32_bf16 v[10:13], v[154:157], v[206:209], 0
	v_mfma_f32_16x16x32_bf16 v[62:65], v[150:153], v[182:185], v[62:65]
	v_mfma_f32_16x16x32_bf16 v[58:61], v[158:161], v[182:185], v[58:61]
	v_mfma_f32_16x16x32_bf16 v[46:49], v[150:153], v[190:193], v[46:49]
	v_mfma_f32_16x16x32_bf16 v[42:45], v[158:161], v[190:193], v[42:45]
	v_mfma_f32_16x16x32_bf16 v[30:33], v[150:153], v[202:205], v[30:33]
	v_mfma_f32_16x16x32_bf16 v[26:29], v[158:161], v[202:205], v[26:29]
	v_mfma_f32_16x16x32_bf16 v[14:17], v[150:153], v[210:213], v[14:17]
	v_mfma_f32_16x16x32_bf16 v[10:13], v[158:161], v[210:213], v[10:13]
	s_setprio 0
	s_setprio 1
	v_mfma_f32_16x16x32_bf16 v[54:57], v[162:165], v[178:181], 0
	v_mfma_f32_16x16x32_bf16 v[50:53], v[170:173], v[178:181], 0
	v_mfma_f32_16x16x32_bf16 v[38:41], v[162:165], v[186:189], 0
	v_mfma_f32_16x16x32_bf16 v[34:37], v[170:173], v[186:189], 0
	v_mfma_f32_16x16x32_bf16 v[22:25], v[162:165], v[194:197], 0
	v_mfma_f32_16x16x32_bf16 v[18:21], v[170:173], v[194:197], 0
	v_mfma_f32_16x16x32_bf16 v[6:9], v[162:165], v[206:209], 0
	v_mfma_f32_16x16x32_bf16 v[2:5], v[170:173], v[206:209], 0
	v_mfma_f32_16x16x32_bf16 v[54:57], v[166:169], v[182:185], v[54:57]
	v_mfma_f32_16x16x32_bf16 v[50:53], v[174:177], v[182:185], v[50:53]
	v_mfma_f32_16x16x32_bf16 v[38:41], v[166:169], v[190:193], v[38:41]
	v_mfma_f32_16x16x32_bf16 v[34:37], v[174:177], v[190:193], v[34:37]
	v_mfma_f32_16x16x32_bf16 v[22:25], v[166:169], v[202:205], v[22:25]
	v_mfma_f32_16x16x32_bf16 v[18:21], v[174:177], v[202:205], v[18:21]
	v_mfma_f32_16x16x32_bf16 v[6:9], v[166:169], v[210:213], v[6:9]
	v_mfma_f32_16x16x32_bf16 v[2:5], v[174:177], v[210:213], v[2:5]
	s_setprio 0
	s_barrier
	s_add_i32 s47, 0, 0x18000
	v_add_u32_e32 v145, s47, v142
	s_add_i32 s48, 0, 0x1c000
	ds_read_b128 v[146:149], v145
	ds_read_b128 v[150:153], v145 offset:1024
	ds_read_b128 v[154:157], v145 offset:2048
	ds_read_b128 v[158:161], v145 offset:3072
	v_add_u32_e32 v145, s48, v142
	ds_read_b128 v[162:165], v145
	ds_read_b128 v[166:169], v145 offset:1024
	ds_read_b128 v[170:173], v145 offset:2048
	ds_read_b128 v[174:177], v145 offset:3072
	s_add_u32 s4, s4, s8
	s_addc_u32 s5, s5, s9
	s_mov_b32 m0, s36
	v_lshl_add_u64 v[238:239], s[4:5], 0, v[132:133]
	ds_read_b128 v[178:181], v144 offset:32768
	ds_read_b128 v[182:185], v144 offset:33792
	ds_read_b128 v[186:189], v144 offset:34816
	ds_read_b128 v[190:193], v144 offset:35840
	ds_read_b128 v[194:197], v144 offset:36864
	ds_read_b128 v[202:205], v144 offset:37888
	ds_read_b128 v[206:209], v144 offset:38912
	ds_read_b128 v[210:213], v144 offset:39936
	global_load_lds_dwordx4 v[238:239], off
	v_lshl_add_u64 v[238:239], s[4:5], 0, v[134:135]
	s_mov_b32 m0, s37
	s_nop 0
	global_load_lds_dwordx4 v[238:239], off
	s_waitcnt vmcnt(8)
	s_waitcnt lgkmcnt(0)
	s_barrier
	s_setprio 1
	s_waitcnt lgkmcnt(0)
	v_mfma_f32_16x16x32_bf16 v[126:129], v[146:149], v[178:181], v[126:129]
	v_mfma_f32_16x16x32_bf16 v[122:125], v[154:157], v[178:181], v[122:125]
	v_mfma_f32_16x16x32_bf16 v[110:113], v[146:149], v[186:189], v[110:113]
	v_mfma_f32_16x16x32_bf16 v[106:109], v[154:157], v[186:189], v[106:109]
	v_mfma_f32_16x16x32_bf16 v[94:97], v[146:149], v[194:197], v[94:97]
	v_mfma_f32_16x16x32_bf16 v[90:93], v[154:157], v[194:197], v[90:93]
	v_mfma_f32_16x16x32_bf16 v[78:81], v[146:149], v[206:209], v[78:81]
	v_mfma_f32_16x16x32_bf16 v[74:77], v[154:157], v[206:209], v[74:77]
	v_mfma_f32_16x16x32_bf16 v[126:129], v[150:153], v[182:185], v[126:129]
	v_mfma_f32_16x16x32_bf16 v[122:125], v[158:161], v[182:185], v[122:125]
	v_mfma_f32_16x16x32_bf16 v[110:113], v[150:153], v[190:193], v[110:113]
	v_mfma_f32_16x16x32_bf16 v[106:109], v[158:161], v[190:193], v[106:109]
	v_mfma_f32_16x16x32_bf16 v[94:97], v[150:153], v[202:205], v[94:97]
	v_mfma_f32_16x16x32_bf16 v[90:93], v[158:161], v[202:205], v[90:93]
	v_mfma_f32_16x16x32_bf16 v[78:81], v[150:153], v[210:213], v[78:81]
	v_mfma_f32_16x16x32_bf16 v[74:77], v[158:161], v[210:213], v[74:77]
	s_setprio 0
	s_setprio 1
	v_mfma_f32_16x16x32_bf16 v[118:121], v[162:165], v[178:181], v[118:121]
	v_mfma_f32_16x16x32_bf16 v[114:117], v[170:173], v[178:181], v[114:117]
	v_mfma_f32_16x16x32_bf16 v[102:105], v[162:165], v[186:189], v[102:105]
	v_mfma_f32_16x16x32_bf16 v[98:101], v[170:173], v[186:189], v[98:101]
	v_mfma_f32_16x16x32_bf16 v[86:89], v[162:165], v[194:197], v[86:89]
	v_mfma_f32_16x16x32_bf16 v[82:85], v[170:173], v[194:197], v[82:85]
	v_mfma_f32_16x16x32_bf16 v[70:73], v[162:165], v[206:209], v[70:73]
	v_mfma_f32_16x16x32_bf16 v[66:69], v[170:173], v[206:209], v[66:69]
	v_mfma_f32_16x16x32_bf16 v[118:121], v[166:169], v[182:185], v[118:121]
	v_mfma_f32_16x16x32_bf16 v[114:117], v[174:177], v[182:185], v[114:117]
	v_mfma_f32_16x16x32_bf16 v[102:105], v[166:169], v[190:193], v[102:105]
	v_mfma_f32_16x16x32_bf16 v[98:101], v[174:177], v[190:193], v[98:101]
	v_mfma_f32_16x16x32_bf16 v[86:89], v[166:169], v[202:205], v[86:89]
	v_mfma_f32_16x16x32_bf16 v[82:85], v[174:177], v[202:205], v[82:85]
	v_mfma_f32_16x16x32_bf16 v[70:73], v[166:169], v[210:213], v[70:73]
	v_mfma_f32_16x16x32_bf16 v[66:69], v[174:177], v[210:213], v[66:69]
	s_setprio 0
	s_barrier
	s_add_i32 s4, s47, s31
	v_lshl_add_u64 v[214:215], v[214:215], 0, s[94:95]
	s_mov_b32 m0, s4
	ds_read_b128 v[178:181], v144 offset:49152
	ds_read_b128 v[182:185], v144 offset:50176
	ds_read_b128 v[186:189], v144 offset:51200
	ds_read_b128 v[190:193], v144 offset:52224
	ds_read_b128 v[194:197], v144 offset:53248
	ds_read_b128 v[202:205], v144 offset:54272
	ds_read_b128 v[206:209], v144 offset:55296
	ds_read_b128 v[210:213], v144 offset:56320
	global_load_lds_dwordx4 v[214:215], off
	v_lshl_add_u64 v[214:215], v[216:217], 0, s[94:95]
	s_add_i32 m0, s4, 0x2000
	s_add_i32 s4, s48, s31
	global_load_lds_dwordx4 v[214:215], off
	v_lshl_add_u64 v[214:215], v[218:219], 0, s[94:95]
	s_mov_b32 m0, s4
	s_nop 0
	global_load_lds_dwordx4 v[214:215], off
	v_lshl_add_u64 v[214:215], v[220:221], 0, s[94:95]
	s_add_i32 m0, s4, 0x2000
	s_nop 0
	global_load_lds_dwordx4 v[214:215], off
	v_lshl_add_u64 v[214:215], v[234:235], 0, s[94:95]
	s_mov_b32 m0, s39
	s_nop 0
	global_load_lds_dwordx4 v[214:215], off
	v_lshl_add_u64 v[214:215], v[236:237], 0, s[94:95]
	s_mov_b32 m0, s40
	s_nop 0
	global_load_lds_dwordx4 v[214:215], off
	s_waitcnt vmcnt(8)
	s_waitcnt lgkmcnt(0)
	s_barrier
	s_setprio 1
	s_waitcnt lgkmcnt(0)
	v_mfma_f32_16x16x32_bf16 v[62:65], v[146:149], v[178:181], v[62:65]
	v_mfma_f32_16x16x32_bf16 v[58:61], v[154:157], v[178:181], v[58:61]
	v_mfma_f32_16x16x32_bf16 v[46:49], v[146:149], v[186:189], v[46:49]
	v_mfma_f32_16x16x32_bf16 v[42:45], v[154:157], v[186:189], v[42:45]
	v_mfma_f32_16x16x32_bf16 v[30:33], v[146:149], v[194:197], v[30:33]
	v_mfma_f32_16x16x32_bf16 v[26:29], v[154:157], v[194:197], v[26:29]
	v_mfma_f32_16x16x32_bf16 v[14:17], v[146:149], v[206:209], v[14:17]
	v_mfma_f32_16x16x32_bf16 v[10:13], v[154:157], v[206:209], v[10:13]
	v_mfma_f32_16x16x32_bf16 v[62:65], v[150:153], v[182:185], v[62:65]
	v_mfma_f32_16x16x32_bf16 v[58:61], v[158:161], v[182:185], v[58:61]
	v_mfma_f32_16x16x32_bf16 v[46:49], v[150:153], v[190:193], v[46:49]
	v_mfma_f32_16x16x32_bf16 v[42:45], v[158:161], v[190:193], v[42:45]
	v_mfma_f32_16x16x32_bf16 v[30:33], v[150:153], v[202:205], v[30:33]
	v_mfma_f32_16x16x32_bf16 v[26:29], v[158:161], v[202:205], v[26:29]
	v_mfma_f32_16x16x32_bf16 v[14:17], v[150:153], v[210:213], v[14:17]
	v_mfma_f32_16x16x32_bf16 v[10:13], v[158:161], v[210:213], v[10:13]
	s_setprio 0
	s_setprio 1
	v_mfma_f32_16x16x32_bf16 v[54:57], v[162:165], v[178:181], v[54:57]
	v_mfma_f32_16x16x32_bf16 v[50:53], v[170:173], v[178:181], v[50:53]
	v_mfma_f32_16x16x32_bf16 v[38:41], v[162:165], v[186:189], v[38:41]
	v_mfma_f32_16x16x32_bf16 v[34:37], v[170:173], v[186:189], v[34:37]
	v_mfma_f32_16x16x32_bf16 v[22:25], v[162:165], v[194:197], v[22:25]
	v_mfma_f32_16x16x32_bf16 v[18:21], v[170:173], v[194:197], v[18:21]
	v_mfma_f32_16x16x32_bf16 v[6:9], v[162:165], v[206:209], v[6:9]
	v_mfma_f32_16x16x32_bf16 v[2:5], v[170:173], v[206:209], v[2:5]
	v_mfma_f32_16x16x32_bf16 v[54:57], v[166:169], v[182:185], v[54:57]
	v_mfma_f32_16x16x32_bf16 v[50:53], v[174:177], v[182:185], v[50:53]
	v_mfma_f32_16x16x32_bf16 v[38:41], v[166:169], v[190:193], v[38:41]
	v_mfma_f32_16x16x32_bf16 v[34:37], v[174:177], v[190:193], v[34:37]
	v_mfma_f32_16x16x32_bf16 v[22:25], v[166:169], v[202:205], v[22:25]
	v_mfma_f32_16x16x32_bf16 v[18:21], v[174:177], v[202:205], v[18:21]
	v_mfma_f32_16x16x32_bf16 v[6:9], v[166:169], v[210:213], v[6:9]
	v_mfma_f32_16x16x32_bf16 v[2:5], v[174:177], v[210:213], v[2:5]
	s_setprio 0
	s_barrier
	s_add_u32 s24, s24, 0x100
	s_addc_u32 s25, s25, 0
	s_add_u32 s26, s26, 0x100
	s_addc_u32 s27, s27, 0
	s_cmp_ge_i32 s46, s38
	s_mov_b32 s4, s46
	s_cbranch_scc1 .LBB0_841

.LBB0_843:
	v_med3_f32 v145, v126, s63, v230
	v_med3_f32 v127, v127, s63, v230
	v_mov_b32_e32 v126, v1
	v_cvt_pk_fp8_f32 v126, v145, v127
	v_med3_f32 v128, v128, s63, v230
	v_med3_f32 v129, v129, s63, v230
	v_med3_f32 v114, v114, s63, v230
	v_cvt_pk_fp8_f32 v126, v128, v129 op_sel:[0,0,1]
	v_med3_f32 v115, v115, s63, v230
	v_mov_b32_e32 v129, v1
	v_cvt_pk_fp8_f32 v129, v114, v115
	v_med3_f32 v115, v117, s63, v230
	v_med3_f32 v117, v110, s63, v230
	v_med3_f32 v111, v111, s63, v230
	v_mov_b32_e32 v110, v1
	v_cvt_pk_fp8_f32 v110, v117, v111
	v_med3_f32 v112, v112, s63, v230
	v_med3_f32 v113, v113, s63, v230
	v_med3_f32 v106, v106, s63, v230
	v_med3_f32 v107, v107, s63, v230
	v_mov_b32_e32 v111, v1
	v_cvt_pk_fp8_f32 v110, v112, v113 op_sel:[0,0,1]
	v_med3_f32 v102, v102, s63, v230
	v_med3_f32 v103, v103, s63, v230
	v_mov_b32_e32 v112, v1
	v_med3_f32 v98, v98, s63, v230
	v_med3_f32 v99, v99, s63, v230
	v_mov_b32_e32 v113, v1
	v_cvt_pk_fp8_f32 v111, v106, v107
	v_cvt_pk_fp8_f32 v112, v102, v103
	v_cvt_pk_fp8_f32 v113, v98, v99
	v_lshl_add_u32 v146, s43, 8, v141
	v_med3_f32 v114, v116, s63, v230
	v_or_b32_e32 v116, 16, v146
	v_med3_f32 v106, v108, s63, v230
	v_med3_f32 v107, v109, s63, v230
	v_med3_f32 v102, v104, s63, v230
	v_med3_f32 v103, v105, s63, v230
	v_med3_f32 v98, v100, s63, v230
	v_med3_f32 v99, v101, s63, v230
	v_cvt_pk_fp8_f32 v111, v106, v107 op_sel:[0,0,1]
	v_cvt_pk_fp8_f32 v112, v102, v103 op_sel:[0,0,1]
	v_cvt_pk_fp8_f32 v113, v98, v99 op_sel:[0,0,1]
	v_ashrrev_i32_e32 v117, 31, v116
	v_lshl_add_u32 v148, s45, 8, v143
	v_lshlrev_b64 v[98:99], 11, v[116:117]
	v_ashrrev_i32_e32 v149, 31, v148
	v_lshl_add_u64 v[98:99], s[10:11], 0, v[98:99]
	v_lshl_add_u64 v[98:99], v[98:99], 0, v[148:149]
	global_store_dwordx4 v[98:99], v[110:113], off
	v_med3_f32 v99, v94, s63, v230
	v_med3_f32 v95, v95, s63, v230
	v_mov_b32_e32 v94, v1
	v_cvt_pk_fp8_f32 v94, v99, v95
	v_med3_f32 v96, v96, s63, v230
	v_med3_f32 v97, v97, s63, v230
	v_med3_f32 v90, v90, s63, v230
	v_med3_f32 v91, v91, s63, v230
	v_mov_b32_e32 v95, v1
	v_cvt_pk_fp8_f32 v94, v96, v97 op_sel:[0,0,1]
	v_med3_f32 v86, v86, s63, v230
	v_med3_f32 v87, v87, s63, v230
	v_mov_b32_e32 v96, v1
	v_med3_f32 v82, v82, s63, v230
	v_med3_f32 v83, v83, s63, v230
	v_mov_b32_e32 v97, v1
	v_cvt_pk_fp8_f32 v95, v90, v91
	v_cvt_pk_fp8_f32 v96, v86, v87
	v_cvt_pk_fp8_f32 v97, v82, v83
	v_or_b32_e32 v98, 32, v146
	v_med3_f32 v90, v92, s63, v230
	v_med3_f32 v91, v93, s63, v230
	v_med3_f32 v86, v88, s63, v230
	v_med3_f32 v87, v89, s63, v230
	v_med3_f32 v82, v84, s63, v230
	v_med3_f32 v83, v85, s63, v230
	v_cvt_pk_fp8_f32 v95, v90, v91 op_sel:[0,0,1]
	v_cvt_pk_fp8_f32 v96, v86, v87 op_sel:[0,0,1]
	v_cvt_pk_fp8_f32 v97, v82, v83 op_sel:[0,0,1]
	v_ashrrev_i32_e32 v99, 31, v98
	v_lshlrev_b64 v[82:83], 11, v[98:99]
	v_lshl_add_u64 v[82:83], s[10:11], 0, v[82:83]
	v_lshl_add_u64 v[82:83], v[82:83], 0, v[148:149]
	global_store_dwordx4 v[82:83], v[94:97], off
	v_med3_f32 v83, v78, s63, v230
	v_med3_f32 v79, v79, s63, v230
	v_mov_b32_e32 v78, v1
	v_cvt_pk_fp8_f32 v78, v83, v79
	v_med3_f32 v80, v80, s63, v230
	v_med3_f32 v81, v81, s63, v230
	v_med3_f32 v74, v74, s63, v230
	v_med3_f32 v75, v75, s63, v230
	v_mov_b32_e32 v79, v1
	v_cvt_pk_fp8_f32 v78, v80, v81 op_sel:[0,0,1]
	v_med3_f32 v70, v70, s63, v230
	v_med3_f32 v71, v71, s63, v230
	v_mov_b32_e32 v80, v1
	v_med3_f32 v66, v66, s63, v230
	v_med3_f32 v67, v67, s63, v230
	v_mov_b32_e32 v81, v1
	v_cvt_pk_fp8_f32 v79, v74, v75
	v_cvt_pk_fp8_f32 v80, v70, v71
	v_cvt_pk_fp8_f32 v81, v66, v67
	v_or_b32_e32 v82, 48, v146
	v_med3_f32 v74, v76, s63, v230
	v_med3_f32 v75, v77, s63, v230
	v_med3_f32 v70, v72, s63, v230
	v_med3_f32 v71, v73, s63, v230
	v_med3_f32 v66, v68, s63, v230
	v_med3_f32 v67, v69, s63, v230
	v_cvt_pk_fp8_f32 v79, v74, v75 op_sel:[0,0,1]
	v_cvt_pk_fp8_f32 v80, v70, v71 op_sel:[0,0,1]
	v_cvt_pk_fp8_f32 v81, v66, v67 op_sel:[0,0,1]
	v_ashrrev_i32_e32 v83, 31, v82
	v_lshlrev_b64 v[66:67], 11, v[82:83]
	v_lshl_add_u64 v[66:67], s[10:11], 0, v[66:67]
	v_lshl_add_u64 v[66:67], v[66:67], 0, v[148:149]
	global_store_dwordx4 v[66:67], v[78:81], off
	v_med3_f32 v66, v62, s63, v230
	v_med3_f32 v63, v63, s63, v230
	v_mov_b32_e32 v62, v1
	v_cvt_pk_fp8_f32 v62, v66, v63
	v_med3_f32 v64, v64, s63, v230
	v_med3_f32 v65, v65, s63, v230
	v_med3_f32 v58, v58, s63, v230
	v_med3_f32 v59, v59, s63, v230
	v_mov_b32_e32 v63, v1
	v_cvt_pk_fp8_f32 v62, v64, v65 op_sel:[0,0,1]
	v_med3_f32 v54, v54, s63, v230
	v_med3_f32 v55, v55, s63, v230
	v_mov_b32_e32 v64, v1
	v_med3_f32 v50, v50, s63, v230
	v_med3_f32 v51, v51, s63, v230
	v_mov_b32_e32 v65, v1
	v_cvt_pk_fp8_f32 v63, v58, v59
	v_cvt_pk_fp8_f32 v64, v54, v55
	v_cvt_pk_fp8_f32 v65, v50, v51
	v_ashrrev_i32_e32 v147, 31, v146
	v_cvt_pk_fp8_f32 v129, v114, v115 op_sel:[0,0,1]
	v_lshlrev_b64 v[114:115], 11, v[146:147]
	v_med3_f32 v58, v60, s63, v230
	v_med3_f32 v59, v61, s63, v230
	v_med3_f32 v54, v56, s63, v230
	v_med3_f32 v55, v57, s63, v230
	v_med3_f32 v50, v52, s63, v230
	v_med3_f32 v51, v53, s63, v230
	v_lshl_add_u64 v[114:115], s[10:11], 0, v[114:115]
	v_cvt_pk_fp8_f32 v63, v58, v59 op_sel:[0,0,1]
	v_cvt_pk_fp8_f32 v64, v54, v55 op_sel:[0,0,1]
	v_cvt_pk_fp8_f32 v65, v50, v51 op_sel:[0,0,1]
	v_lshl_add_u64 v[114:115], v[114:115], 0, v[148:149]
	s_mov_b32 s4, 0x40000
	v_add_co_u32_e32 v50, vcc, s4, v114
	v_med3_f32 v47, v47, s63, v230
	s_nop 0
	v_addc_co_u32_e32 v51, vcc, 0, v115, vcc
	global_store_dwordx4 v[50:51], v[62:65], off
	v_med3_f32 v50, v46, s63, v230
	v_mov_b32_e32 v46, v1
	v_cvt_pk_fp8_f32 v46, v50, v47
	v_med3_f32 v48, v48, s63, v230
	v_med3_f32 v49, v49, s63, v230
	v_med3_f32 v42, v42, s63, v230
	v_med3_f32 v43, v43, s63, v230
	v_mov_b32_e32 v47, v1
	v_cvt_pk_fp8_f32 v46, v48, v49 op_sel:[0,0,1]
	v_med3_f32 v38, v38, s63, v230
	v_med3_f32 v39, v39, s63, v230
	v_mov_b32_e32 v48, v1
	v_med3_f32 v34, v34, s63, v230
	v_med3_f32 v35, v35, s63, v230
	v_mov_b32_e32 v49, v1
	v_cvt_pk_fp8_f32 v47, v42, v43
	v_cvt_pk_fp8_f32 v48, v38, v39
	v_cvt_pk_fp8_f32 v49, v34, v35
	v_med3_f32 v42, v44, s63, v230
	v_med3_f32 v43, v45, s63, v230
	v_med3_f32 v38, v40, s63, v230
	v_med3_f32 v39, v41, s63, v230
	v_med3_f32 v34, v36, s63, v230
	v_med3_f32 v35, v37, s63, v230
	v_cvt_pk_fp8_f32 v47, v42, v43 op_sel:[0,0,1]
	v_cvt_pk_fp8_f32 v48, v38, v39 op_sel:[0,0,1]
	v_cvt_pk_fp8_f32 v49, v34, v35 op_sel:[0,0,1]
	s_mov_b32 s4, 0x48000
	v_add_co_u32_e32 v34, vcc, s4, v114
	v_med3_f32 v31, v31, s63, v230
	s_nop 0
	v_addc_co_u32_e32 v35, vcc, 0, v115, vcc
	global_store_dwordx4 v[34:35], v[46:49], off
	v_med3_f32 v34, v30, s63, v230
	v_mov_b32_e32 v30, v1
	v_cvt_pk_fp8_f32 v30, v34, v31
	v_med3_f32 v32, v32, s63, v230
	v_med3_f32 v33, v33, s63, v230
	v_med3_f32 v26, v26, s63, v230
	v_med3_f32 v27, v27, s63, v230
	v_mov_b32_e32 v31, v1
	v_cvt_pk_fp8_f32 v30, v32, v33 op_sel:[0,0,1]
	v_med3_f32 v22, v22, s63, v230
	v_med3_f32 v23, v23, s63, v230
	v_mov_b32_e32 v32, v1
	v_med3_f32 v18, v18, s63, v230
	v_med3_f32 v19, v19, s63, v230
	v_mov_b32_e32 v33, v1
	v_cvt_pk_fp8_f32 v31, v26, v27
	v_cvt_pk_fp8_f32 v32, v22, v23
	v_cvt_pk_fp8_f32 v33, v18, v19
	v_med3_f32 v26, v28, s63, v230
	v_med3_f32 v27, v29, s63, v230
	v_med3_f32 v22, v24, s63, v230
	v_med3_f32 v23, v25, s63, v230
	v_med3_f32 v18, v20, s63, v230
	v_med3_f32 v19, v21, s63, v230
	v_cvt_pk_fp8_f32 v31, v26, v27 op_sel:[0,0,1]
	v_cvt_pk_fp8_f32 v32, v22, v23 op_sel:[0,0,1]
	v_cvt_pk_fp8_f32 v33, v18, v19 op_sel:[0,0,1]
	s_mov_b32 s4, 0x50000
	v_add_co_u32_e32 v18, vcc, s4, v114
	v_med3_f32 v15, v15, s63, v230
	s_nop 0
	v_addc_co_u32_e32 v19, vcc, 0, v115, vcc
	global_store_dwordx4 v[18:19], v[30:33], off
	v_med3_f32 v18, v14, s63, v230
	v_mov_b32_e32 v14, v1
	v_cvt_pk_fp8_f32 v14, v18, v15
	v_med3_f32 v16, v16, s63, v230
	v_med3_f32 v17, v17, s63, v230
	v_med3_f32 v122, v122, s63, v230
	v_med3_f32 v123, v123, s63, v230
	v_mov_b32_e32 v127, v1
	v_med3_f32 v118, v118, s63, v230
	v_med3_f32 v119, v119, s63, v230
	v_mov_b32_e32 v128, v1
	v_med3_f32 v10, v10, s63, v230
	v_med3_f32 v11, v11, s63, v230
	v_mov_b32_e32 v15, v1
	v_cvt_pk_fp8_f32 v14, v16, v17 op_sel:[0,0,1]
	v_med3_f32 v6, v6, s63, v230
	v_med3_f32 v7, v7, s63, v230
	v_mov_b32_e32 v16, v1
	v_med3_f32 v2, v2, s63, v230
	v_med3_f32 v3, v3, s63, v230
	v_mov_b32_e32 v17, v1
	v_cvt_pk_fp8_f32 v127, v122, v123
	v_cvt_pk_fp8_f32 v128, v118, v119
	v_cvt_pk_fp8_f32 v15, v10, v11
	v_cvt_pk_fp8_f32 v16, v6, v7
	v_cvt_pk_fp8_f32 v17, v2, v3
	v_med3_f32 v122, v124, s63, v230
	v_med3_f32 v123, v125, s63, v230
	v_med3_f32 v118, v120, s63, v230
	v_med3_f32 v119, v121, s63, v230
	v_med3_f32 v10, v12, s63, v230
	v_med3_f32 v11, v13, s63, v230
	v_med3_f32 v6, v8, s63, v230
	v_med3_f32 v7, v9, s63, v230
	v_med3_f32 v2, v4, s63, v230
	v_med3_f32 v3, v5, s63, v230
	v_cvt_pk_fp8_f32 v127, v122, v123 op_sel:[0,0,1]
	v_cvt_pk_fp8_f32 v128, v118, v119 op_sel:[0,0,1]
	v_cvt_pk_fp8_f32 v15, v10, v11 op_sel:[0,0,1]
	v_cvt_pk_fp8_f32 v16, v6, v7 op_sel:[0,0,1]
	v_cvt_pk_fp8_f32 v17, v2, v3 op_sel:[0,0,1]
	v_add_co_u32_e32 v2, vcc, 0x58000, v114
	s_mov_b64 s[4:5], -1
	s_nop 0
	v_addc_co_u32_e32 v3, vcc, 0, v115, vcc
	s_andn2_b64 vcc, exec, s[6:7]
	global_store_dwordx4 v[114:115], v[126:129], off
	global_store_dwordx4 v[2:3], v[14:17], off
	s_waitcnt vmcnt(8)
	s_cbranch_vccnz .LBB0_835
	s_andn2_b64 vcc, exec, s[12:13]
	s_cbranch_vccnz .LBB0_834
	s_barrier
	s_branch .LBB0_834
